# MoE-down epilogue: hoist the 16 x read-back loads to the epilogue top; plus router pass-2 pipelined loads, attention V LDS layout
# speedup vs baseline: 1.0238x; 1.0238x over previous
.LBB0_491:
	s_or_b64 exec, exec, s[20:21]
	global_load_dwordx4 v[30:33], v[148:149], off offset:128
	s_movk_i32 s19, 0xd0
	v_mul_lo_u32 v35, v161, s19
	v_lshl_add_u32 v188, v37, 4, v35
	v_add_u32_e32 v35, 0, v188
	v_mul_lo_u32 v192, v187, s19
	s_waitcnt vmcnt(3)
	ds_write_b128 v35, v[18:21]
	s_and_saveexec_b64 s[20:21], s[38:39]
	v_lshlrev_b32_e32 v18, 4, v191
	v_add3_u32 v18, 0, v18, v192
	ds_write_b128 v18, v[116:119]
	s_or_b64 exec, exec, s[20:21]
	s_movk_i32 s19, 0x90
	v_mul_lo_u32 v18, v34, s19
	v_and_b32_e32 v189, 6, v194
	v_lshl_add_u32 v189, v189, 4, v18
	v_and_b32_e32 v18, 1, v194
	v_lshl_add_u32 v189, v18, 3, v189
	v_add_u32_e32 v18, 0, v189
	s_waitcnt vmcnt(2)
	ds_write_b64 v18, v[22:23] offset:13312
	ds_write_b64 v18, v[24:25] offset:13328
	s_waitcnt vmcnt(1)
	ds_write_b128 v35, v[26:29] offset:22528
	s_and_saveexec_b64 s[20:21], s[38:39]
	v_lshlrev_b32_e32 v19, 4, v191
	v_add3_u32 v19, 0, v19, v192
	ds_write_b128 v19, v[120:123] offset:22528
	s_or_b64 exec, exec, s[20:21]
	s_lshl_b32 s24, s22, 2
	s_ashr_i32 s19, s25, 1
	s_add_i32 s19, s19, s24
	s_ashr_i32 s19, s19, 1
	s_mov_b64 s[20:21], -1
	s_cmp_gt_i32 s19, 0
	v_mul_u32_u24_e32 v114, 0x68, v193
	s_waitcnt vmcnt(0)
	ds_write_b64 v18, v[30:31] offset:35840
	ds_write_b64 v18, v[32:33] offset:35856
	s_waitcnt lgkmcnt(0)
	s_barrier
	s_cbranch_scc1 .LBB0_497
	v_mul_u32_u24_e32 v50, 0x68, v193
	s_mov_b64 s[20:21], 0

.LBB0_499:
	s_or_b64 exec, exec, s[22:23]
	s_add_i32 s26, s26, 2
	s_cmp_lg_u32 s19, s27
	s_waitcnt vmcnt(0)
	ds_write_b64 v62, v[94:95] offset:35840
	ds_write_b64 v62, v[96:97] offset:35856
	v_add_f32_e32 v66, v66, v67
	v_add_f32_e32 v80, v80, v81
	v_add_f32_e32 v68, v68, v69
	v_add_f32_e32 v52, v52, v53
	v_add_f32_e32 v70, v70, v71
	v_add_f32_e32 v50, v50, v51
	v_add_f32_e32 v72, v72, v73
	v_add_f32_e32 v54, v54, v55
	v_add_f32_e32 v182, v182, v183
	v_add_f32_e32 v184, v184, v185
	v_add_f32_e32 v76, v76, v77
	v_add_f32_e32 v58, v58, v59
	v_add_f32_e32 v74, v74, v75
	v_add_f32_e32 v56, v56, v57
	v_add_f32_e32 v78, v78, v79
	v_add_f32_e32 v60, v60, v61
	v_add_f32_e32 v66, v66, v80
	v_add_f32_e32 v68, v68, v52
	v_add_f32_e32 v70, v70, v50
	v_add_f32_e32 v72, v72, v54
	v_add_f32_e32 v182, v182, v184
	v_add_f32_e32 v76, v76, v58
	v_add_f32_e32 v74, v74, v56
	v_add_f32_e32 v78, v78, v60
	v_add_f32_e32 v66, v66, v68
	v_add_f32_e32 v70, v70, v72
	v_add_f32_e32 v182, v182, v76
	v_add_f32_e32 v74, v74, v78
	v_add_f32_e32 v162, v162, v66
	v_add_f32_e32 v163, v163, v70
	v_add_f32_e32 v162, v162, v182
	v_add_f32_e32 v163, v163, v74
	s_waitcnt lgkmcnt(0)
	s_barrier
	s_cbranch_scc0 .LBB0_509

.LBB0_504:
	s_or_b64 exec, exec, s[22:23]
	s_and_b32 s21, s26, 2
	s_mulk_i32 s21, 0x5800
	v_add_u32_e32 v96, s21, v195
	v_lshlrev_b32_e32 v97, 1, v160
	v_add_u32_e32 v112, v96, v97
	ds_read_b128 v[50:53], v112
	ds_read_b128 v[100:103], v112 offset:32
	ds_read_b128 v[104:107], v112 offset:6656
	ds_read_b128 v[108:111], v112 offset:6688
	ds_read_b128 v[164:167], v112 offset:64
	ds_read_b128 v[168:171], v112 offset:96
	ds_read_b128 v[176:179], v112 offset:6720
	ds_read_b128 v[198:201], v112 offset:6752
	ds_read_b128 v[202:205], v112 offset:128
	v_add_u32_e32 v96, v96, v197
	s_waitcnt lgkmcnt(8)
	v_mfma_f32_32x32x16_bf16 v[66:81], v[50:53], v[144:147], v[2:17]
	v_lshl_add_u32 v206, v150, 2, v96
	v_add_u32_e32 v175, 0x3000, v206
	v_add_u32_e32 v182, 0x4000, v206
	v_add3_u32 v207, v96, v196, v97
	v_add_u32_e32 v211, 0x9800, v206
	v_add_u32_e32 v210, 0x8800, v206
	s_add_i32 s27, s27, 1
	s_waitcnt lgkmcnt(7)
	v_mfma_f32_32x32x16_bf16 v[66:81], v[100:103], v[140:143], v[66:81]
	s_bitcmp1_b32 s27, 0
	s_cselect_b32 s21, 0xb000, 0
	s_add_i32 s21, s21, 0
	s_waitcnt lgkmcnt(6)
	v_mfma_f32_32x32x16_bf16 v[50:65], v[104:107], v[144:147], v[2:17]
	ds_read_b128 v[100:103], v112 offset:160
	s_waitcnt lgkmcnt(5)
	v_mfma_f32_32x32x16_bf16 v[66:81], v[164:167], v[136:139], v[66:81]
	v_mfma_f32_32x32x16_bf16 v[50:65], v[108:111], v[140:143], v[50:65]
	ds_read_b128 v[104:107], v112 offset:6784
	s_waitcnt lgkmcnt(5)
	v_mfma_f32_32x32x16_bf16 v[66:81], v[168:171], v[132:135], v[66:81]
	ds_read_b128 v[108:111], v112 offset:6816
	s_waitcnt lgkmcnt(5)
	v_mfma_f32_32x32x16_bf16 v[50:65], v[176:179], v[136:139], v[50:65]
	s_waitcnt lgkmcnt(3)
	v_mfma_f32_32x32x16_bf16 v[66:81], v[202:205], v[128:131], v[66:81]
	v_mfma_f32_32x32x16_bf16 v[50:65], v[198:201], v[132:135], v[50:65]
	s_waitcnt lgkmcnt(2)
	v_mfma_f32_32x32x16_bf16 v[66:81], v[100:103], v[124:127], v[66:81]
	s_waitcnt lgkmcnt(1)
	v_mfma_f32_32x32x16_bf16 v[50:65], v[104:107], v[128:131], v[50:65]
	s_nop 9
	v_exp_f32_e32 v100, v66
	v_exp_f32_e32 v101, v67
	v_exp_f32_e32 v102, v68
	v_exp_f32_e32 v103, v69
	ds_read_b128 v[66:69], v175 offset:1024
	v_exp_f32_e32 v104, v70
	v_exp_f32_e32 v105, v71
	v_exp_f32_e32 v106, v72
	v_exp_f32_e32 v107, v73
	v_cvt_pk_bf16_f32 v70, v100, v101
	v_cvt_pk_bf16_f32 v71, v102, v103
	v_cvt_pk_bf16_f32 v72, v104, v105
	v_cvt_pk_bf16_f32 v73, v106, v107
	s_waitcnt lgkmcnt(1)
	v_mfma_f32_32x32x16_bf16 v[50:65], v[108:111], v[124:127], v[50:65]
	v_exp_f32_e32 v112, v74
	v_exp_f32_e32 v113, v75
	v_exp_f32_e32 v110, v76
	v_exp_f32_e32 v111, v77
	ds_read_b128 v[74:77], v175 offset:1056
	v_exp_f32_e32 v108, v78
	v_exp_f32_e32 v109, v79
	s_waitcnt lgkmcnt(1)
	v_mfma_f32_32x32x16_bf16 v[18:33], v[66:69], v[70:73], v[18:33]
	ds_read_b128 v[66:69], v182 offset:1536
	v_exp_f32_e32 v164, v80
	v_exp_f32_e32 v165, v81
	v_exp_f32_e32 v170, v50
	v_exp_f32_e32 v171, v51
	v_exp_f32_e32 v168, v52
	v_exp_f32_e32 v169, v53
	s_waitcnt lgkmcnt(0)
	v_mfma_f32_32x32x16_bf16 v[34:49], v[66:69], v[70:73], v[34:49]
	v_cvt_pk_bf16_f32 v66, v112, v113
	v_cvt_pk_bf16_f32 v67, v110, v111
	v_cvt_pk_bf16_f32 v68, v108, v109
	v_cvt_pk_bf16_f32 v69, v164, v165
	ds_read_b128 v[50:53], v175 offset:1088
	ds_read_b128 v[70:73], v182 offset:1568
	v_exp_f32_e32 v166, v54
	v_mfma_f32_32x32x16_bf16 v[18:33], v[74:77], v[66:69], v[18:33]
	v_exp_f32_e32 v167, v55
	v_exp_f32_e32 v172, v56
	v_exp_f32_e32 v173, v57
	v_cvt_pk_bf16_f32 v54, v170, v171
	v_cvt_pk_bf16_f32 v55, v168, v169
	v_cvt_pk_bf16_f32 v56, v166, v167
	v_cvt_pk_bf16_f32 v57, v172, v173
	s_waitcnt lgkmcnt(0)
	v_mfma_f32_32x32x16_bf16 v[34:49], v[70:73], v[66:69], v[34:49]
	v_exp_f32_e32 v178, v58
	v_exp_f32_e32 v179, v59
	v_exp_f32_e32 v176, v60
	v_exp_f32_e32 v177, v61
	ds_read_b128 v[58:61], v175 offset:1120
	v_exp_f32_e32 v174, v62
	v_exp_f32_e32 v175, v63
	v_mfma_f32_32x32x16_bf16 v[18:33], v[50:53], v[54:57], v[18:33]
	ds_read_b128 v[50:53], v182 offset:1600
	v_exp_f32_e32 v180, v64
	v_exp_f32_e32 v181, v65
	s_waitcnt lgkmcnt(0)
	v_mfma_f32_32x32x16_bf16 v[34:49], v[50:53], v[54:57], v[34:49]
	ds_read_b128 v[54:57], v182 offset:1632
	v_cvt_pk_bf16_f32 v50, v178, v179
	v_cvt_pk_bf16_f32 v51, v176, v177
	v_cvt_pk_bf16_f32 v52, v174, v175
	v_cvt_pk_bf16_f32 v53, v180, v181
	s_nop 1
	v_mfma_f32_32x32x16_bf16 v[18:33], v[58:61], v[50:53], v[18:33]
	s_waitcnt lgkmcnt(0)
	v_mfma_f32_32x32x16_bf16 v[34:49], v[54:57], v[50:53], v[34:49]
	ds_read_b128 v[50:53], v207 offset:22528
	ds_read_b128 v[182:185], v207 offset:22560
	ds_read_b128 v[198:201], v207 offset:29184
	ds_read_b128 v[202:205], v207 offset:29216
	s_waitcnt lgkmcnt(3)
	v_mfma_f32_32x32x16_bf16 v[66:81], v[50:53], v[144:147], v[2:17]
	v_add_f32_e32 v100, v100, v101
	v_add_f32_e32 v170, v170, v171
	v_add_f32_e32 v102, v102, v103
	s_waitcnt lgkmcnt(1)
	v_mfma_f32_32x32x16_bf16 v[50:65], v[198:201], v[144:147], v[2:17]
	v_add_f32_e32 v168, v168, v169
	v_add_f32_e32 v104, v104, v105
	v_add_f32_e32 v166, v166, v167
	v_mfma_f32_32x32x16_bf16 v[66:81], v[182:185], v[140:143], v[66:81]
	v_add_f32_e32 v106, v106, v107
	v_add_f32_e32 v172, v172, v173
	v_add_f32_e32 v112, v112, v113
	ds_read_b128 v[182:185], v207 offset:22592
	ds_read_b128 v[198:201], v207 offset:22624
	s_waitcnt lgkmcnt(2)
	v_mfma_f32_32x32x16_bf16 v[50:65], v[202:205], v[140:143], v[50:65]
	v_add_f32_e32 v178, v178, v179
	v_add_f32_e32 v110, v110, v111
	v_add_f32_e32 v176, v176, v177
	s_waitcnt lgkmcnt(1)
	v_mfma_f32_32x32x16_bf16 v[66:81], v[182:185], v[136:139], v[66:81]
	v_add_f32_e32 v108, v108, v109
	v_add_f32_e32 v174, v174, v175
	v_add_f32_e32 v164, v164, v165
	ds_read_b128 v[182:185], v207 offset:29248
	ds_read_b128 v[202:205], v207 offset:29280
	s_waitcnt lgkmcnt(1)
	v_mfma_f32_32x32x16_bf16 v[50:65], v[182:185], v[136:139], v[50:65]
	v_add_f32_e32 v180, v180, v181
	v_add_f32_e32 v100, v100, v170
	v_add_f32_e32 v102, v102, v168
	v_mfma_f32_32x32x16_bf16 v[66:81], v[198:201], v[132:135], v[66:81]
	v_add_f32_e32 v104, v104, v166
	v_add_f32_e32 v106, v106, v172
	v_add_f32_e32 v112, v112, v178
	ds_read_b128 v[182:185], v207 offset:22656
	ds_read_b128 v[198:201], v207 offset:22688
	global_load_dwordx4 v[94:97], v[94:95], off offset:128
	s_waitcnt lgkmcnt(1)
	v_mfma_f32_32x32x16_bf16 v[66:81], v[182:185], v[128:131], v[66:81]
	v_add_f32_e32 v110, v110, v176
	v_add_f32_e32 v108, v108, v174
	ds_read_b128 v[182:185], v207 offset:29312
	v_mfma_f32_32x32x16_bf16 v[50:65], v[202:205], v[132:135], v[50:65]
	v_add_f32_e32 v164, v164, v180
	ds_read_b128 v[202:205], v211 offset:1536
	s_waitcnt lgkmcnt(2)
	v_mfma_f32_32x32x16_bf16 v[66:81], v[198:201], v[124:127], v[66:81]
	ds_read_b128 v[198:201], v207 offset:29344
	ds_read_b128 v[206:209], v210 offset:1056
	s_waitcnt lgkmcnt(3)
	v_mfma_f32_32x32x16_bf16 v[50:65], v[182:185], v[128:131], v[50:65]
	v_add_f32_e32 v100, v100, v102
	ds_read_b128 v[182:185], v210 offset:1024
	v_add_f32_e32 v104, v104, v106
	v_add_f32_e32 v112, v112, v110
	v_add_f32_e32 v108, v108, v164
	v_add_f32_e32 v162, v162, v100
	v_add_f32_e32 v163, v163, v104
	v_add_f32_e32 v162, v162, v112
	v_add_f32_e32 v163, v163, v108
	v_exp_f32_e32 v66, v66
	v_exp_f32_e32 v67, v67
	v_exp_f32_e32 v68, v68
	v_exp_f32_e32 v69, v69
	v_exp_f32_e32 v70, v70
	v_exp_f32_e32 v71, v71
	v_exp_f32_e32 v72, v72
	v_exp_f32_e32 v73, v73
	s_waitcnt lgkmcnt(2)
	v_mfma_f32_32x32x16_bf16 v[50:65], v[198:201], v[124:127], v[50:65]
	v_cvt_pk_bf16_f32 v198, v66, v67
	v_cvt_pk_bf16_f32 v199, v68, v69
	v_cvt_pk_bf16_f32 v200, v70, v71
	v_cvt_pk_bf16_f32 v201, v72, v73
	v_exp_f32_e32 v76, v76
	v_exp_f32_e32 v77, v77
	s_nop 5
	v_exp_f32_e32 v52, v52
	v_mfma_f32_32x32x16_bf16 v[34:49], v[202:205], v[198:201], v[34:49]
	ds_read_b128 v[202:205], v211 offset:1568
	v_exp_f32_e32 v53, v53
	s_waitcnt lgkmcnt(1)
	v_mfma_f32_32x32x16_bf16 v[18:33], v[182:185], v[198:201], v[18:33]
	v_exp_f32_e32 v182, v74
	v_exp_f32_e32 v183, v75
	v_exp_f32_e32 v74, v78
	v_exp_f32_e32 v75, v79
	v_exp_f32_e32 v78, v80
	v_exp_f32_e32 v79, v81
	v_cvt_pk_bf16_f32 v198, v182, v183
	v_cvt_pk_bf16_f32 v199, v76, v77
	v_cvt_pk_bf16_f32 v200, v74, v75
	v_cvt_pk_bf16_f32 v201, v78, v79
	v_exp_f32_e32 v80, v50
	v_exp_f32_e32 v81, v51
	v_mfma_f32_32x32x16_bf16 v[18:33], v[206:209], v[198:201], v[18:33]
	ds_read_b128 v[206:209], v210 offset:1088
	v_exp_f32_e32 v50, v54
	v_exp_f32_e32 v51, v55
	v_exp_f32_e32 v54, v56
	v_exp_f32_e32 v55, v57
	v_exp_f32_e32 v184, v58
	v_exp_f32_e32 v185, v59
	s_waitcnt lgkmcnt(1)
	v_mfma_f32_32x32x16_bf16 v[34:49], v[202:205], v[198:201], v[34:49]
	ds_read_b128 v[202:205], v211 offset:1600
	v_cvt_pk_bf16_f32 v198, v80, v81
	v_cvt_pk_bf16_f32 v199, v52, v53
	v_cvt_pk_bf16_f32 v200, v50, v51
	v_cvt_pk_bf16_f32 v201, v54, v55
	v_exp_f32_e32 v58, v60
	v_exp_f32_e32 v59, v61
	s_waitcnt lgkmcnt(1)
	v_mfma_f32_32x32x16_bf16 v[18:33], v[206:209], v[198:201], v[18:33]
	ds_read_b128 v[206:209], v210 offset:1120
	v_exp_f32_e32 v56, v62
	v_exp_f32_e32 v57, v63
	v_exp_f32_e32 v60, v64
	v_exp_f32_e32 v61, v65
	v_add_u32_e32 v63, s21, v188
	v_add_u32_e32 v62, s21, v189
	s_waitcnt lgkmcnt(1)
	v_mfma_f32_32x32x16_bf16 v[34:49], v[202:205], v[198:201], v[34:49]
	ds_read_b128 v[202:205], v211 offset:1632
	v_cvt_pk_bf16_f32 v198, v184, v185
	v_cvt_pk_bf16_f32 v199, v58, v59
	v_cvt_pk_bf16_f32 v200, v56, v57
	v_cvt_pk_bf16_f32 v201, v60, v61
	s_waitcnt vmcnt(3)
	ds_write_b128 v63, v[90:93]
	s_waitcnt lgkmcnt(2)
	v_mfma_f32_32x32x16_bf16 v[18:33], v[206:209], v[198:201], v[18:33]
	s_waitcnt lgkmcnt(1)
	v_mfma_f32_32x32x16_bf16 v[34:49], v[202:205], v[198:201], v[34:49]
	s_and_saveexec_b64 s[22:23], s[0:1]
	s_xor_b64 s[22:23], exec, s[22:23]
	s_cbranch_execz .LBB0_506
	s_waitcnt vmcnt(2)
	ds_write_b64 v62, v[82:83] offset:13312
	ds_write_b64 v62, v[84:85] offset:13328
	s_waitcnt vmcnt(1)
	ds_write_b128 v63, v[86:89] offset:22528
.LBB0_506:
	s_andn2_saveexec_b64 s[22:23], s[22:23]
	s_cbranch_execz .LBB0_499
	v_add_u32_e32 v64, s21, v190
	ds_write_b128 v64, v[116:119]
	s_waitcnt vmcnt(2)
	ds_write_b64 v62, v[82:83] offset:13312
	ds_write_b64 v62, v[84:85] offset:13328
	s_waitcnt vmcnt(1)
	ds_write_b128 v63, v[86:89] offset:22528
	ds_write_b128 v64, v[120:123] offset:22528
	s_branch .LBB0_499

.LBB0_510:
	s_lshl_b32 s23, s19, 1
	s_and_b32 s21, s23, 2
	s_mulk_i32 s21, 0x5800
	s_and_b32 s20, s25, 2
	s_add_i32 s22, s21, 0
	v_lshlrev_b32_e32 v82, 1, v50
	v_lshlrev_b32_e32 v83, 1, v160
	v_lshlrev_b32_e32 v114, 3, v194
	s_cmp_eq_u32 s20, 0
	v_add3_u32 v166, s22, v82, v83
	s_mov_b64 s[20:21], -1
	s_cbranch_scc1 .LBB0_512
	ds_read_b128 v[84:87], v166 offset:6656
	ds_read_b128 v[66:69], v166
	ds_read_b128 v[88:91], v166 offset:32
	s_or_b32 s21, s23, 1
	s_and_b32 s20, s21, 3
	s_mulk_i32 s20, 0x5800
	s_waitcnt lgkmcnt(1)
	v_mfma_f32_32x32x16_bf16 v[50:65], v[66:69], v[144:147], v[2:17]
	s_add_i32 s20, s20, 0
	v_add3_u32 v176, s20, v82, v83
	v_mfma_f32_32x32x16_bf16 v[66:81], v[84:87], v[144:147], v[2:17]
	ds_read_b128 v[84:87], v166 offset:6688
	s_waitcnt lgkmcnt(1)
	v_mfma_f32_32x32x16_bf16 v[50:65], v[88:91], v[140:143], v[50:65]
	s_waitcnt lgkmcnt(0)
	v_mfma_f32_32x32x16_bf16 v[66:81], v[84:87], v[140:143], v[66:81]
	ds_read_b128 v[84:87], v166 offset:64
	ds_read_b128 v[88:91], v166 offset:6720
	s_waitcnt lgkmcnt(1)
	v_mfma_f32_32x32x16_bf16 v[50:65], v[84:87], v[136:139], v[50:65]
	s_waitcnt lgkmcnt(0)
	v_mfma_f32_32x32x16_bf16 v[66:81], v[88:91], v[136:139], v[66:81]
	ds_read_b128 v[84:87], v166 offset:96
	ds_read_b128 v[88:91], v166 offset:6752
	s_waitcnt lgkmcnt(1)
	v_mfma_f32_32x32x16_bf16 v[50:65], v[84:87], v[132:135], v[50:65]
	s_waitcnt lgkmcnt(0)
	v_mfma_f32_32x32x16_bf16 v[66:81], v[88:91], v[132:135], v[66:81]
	ds_read_b128 v[84:87], v166 offset:128
	ds_read_b128 v[88:91], v166 offset:6784
	s_waitcnt lgkmcnt(1)
	v_mfma_f32_32x32x16_bf16 v[50:65], v[84:87], v[128:131], v[50:65]
	s_waitcnt lgkmcnt(0)
	v_mfma_f32_32x32x16_bf16 v[66:81], v[88:91], v[128:131], v[66:81]
	ds_read_b128 v[84:87], v166 offset:160
	ds_read_b128 v[88:91], v166 offset:6816
	s_waitcnt lgkmcnt(1)
	v_mfma_f32_32x32x16_bf16 v[50:65], v[84:87], v[124:127], v[50:65]
	s_waitcnt lgkmcnt(0)
	v_mfma_f32_32x32x16_bf16 v[66:81], v[88:91], v[124:127], v[66:81]
	s_nop 9
	v_exp_f32_e32 v50, v50
	v_exp_f32_e32 v51, v51
	v_exp_f32_e32 v52, v52
	v_exp_f32_e32 v53, v53
	v_exp_f32_e32 v54, v54
	v_exp_f32_e32 v55, v55
	v_exp_f32_e32 v104, v58
	v_exp_f32_e32 v96, v66
	v_exp_f32_e32 v97, v67
	v_exp_f32_e32 v98, v68
	v_exp_f32_e32 v99, v69
	v_exp_f32_e32 v105, v59
	v_pk_add_f32 v[58:59], v[162:163], v[50:51]
	v_exp_f32_e32 v100, v70
	v_exp_f32_e32 v101, v71
	v_pk_add_f32 v[58:59], v[96:97], v[58:59]
	v_exp_f32_e32 v56, v56
	v_exp_f32_e32 v57, v57
	v_pk_add_f32 v[58:59], v[52:53], v[58:59]
	v_cvt_pk_bf16_f32 v84, v50, v51
	v_mul_u32_u24_e32 v50, 0x48, v193
	v_exp_f32_e32 v102, v72
	v_exp_f32_e32 v103, v73
	v_pk_add_f32 v[58:59], v[98:99], v[58:59]
	v_lshlrev_b32_e32 v167, 1, v50
	v_pk_add_f32 v[58:59], v[54:55], v[58:59]
	v_add3_u32 v50, s22, v167, v160
	v_add_u32_e32 v50, v50, v160
	v_exp_f32_e32 v106, v74
	v_exp_f32_e32 v107, v75
	v_pk_add_f32 v[58:59], v[100:101], v[58:59]
	v_add_u32_e32 v174, 0x4000, v50
	v_exp_f32_e32 v108, v60
	v_exp_f32_e32 v109, v61
	v_pk_add_f32 v[58:59], v[56:57], v[58:59]
	ds_read_b128 v[88:91], v174 offset:1536
	v_exp_f32_e32 v110, v76
	v_exp_f32_e32 v111, v77
	v_pk_add_f32 v[58:59], v[102:103], v[58:59]
	v_exp_f32_e32 v112, v62
	v_exp_f32_e32 v113, v63
	v_pk_add_f32 v[58:59], v[104:105], v[58:59]
	v_exp_f32_e32 v168, v78
	v_exp_f32_e32 v169, v79
	v_pk_add_f32 v[58:59], v[106:107], v[58:59]
	v_exp_f32_e32 v170, v64
	v_exp_f32_e32 v171, v65
	v_pk_add_f32 v[58:59], v[108:109], v[58:59]
	v_add_u32_e32 v175, 0x3000, v50
	v_exp_f32_e32 v172, v80
	v_exp_f32_e32 v173, v81
	v_pk_add_f32 v[58:59], v[110:111], v[58:59]
	v_cvt_pk_bf16_f32 v85, v52, v53
	ds_read_b128 v[50:53], v175 offset:1024
	ds_read_b128 v[92:95], v175 offset:1056
	v_pk_add_f32 v[58:59], v[112:113], v[58:59]
	v_cvt_pk_bf16_f32 v86, v54, v55
	v_pk_add_f32 v[58:59], v[168:169], v[58:59]
	v_cvt_pk_bf16_f32 v87, v56, v57
	v_pk_add_f32 v[58:59], v[170:171], v[58:59]
	s_nop 0
	v_pk_add_f32 v[164:165], v[172:173], v[58:59]
	s_waitcnt lgkmcnt(1)
	v_mfma_f32_32x32x16_bf16 v[66:81], v[50:53], v[84:87], v[18:33]
	v_mfma_f32_32x32x16_bf16 v[50:65], v[88:91], v[84:87], v[34:49]
	ds_read_b128 v[88:91], v174 offset:1568
	v_cvt_pk_bf16_f32 v84, v104, v105
	v_cvt_pk_bf16_f32 v85, v108, v109
	v_cvt_pk_bf16_f32 v86, v112, v113
	v_cvt_pk_bf16_f32 v87, v170, v171
	s_waitcnt lgkmcnt(1)
	s_nop 0
	v_mfma_f32_32x32x16_bf16 v[66:81], v[92:95], v[84:87], v[66:81]
	s_waitcnt lgkmcnt(0)
	v_mfma_f32_32x32x16_bf16 v[50:65], v[88:91], v[84:87], v[50:65]
	ds_read_b128 v[88:91], v175 offset:1088
	ds_read_b128 v[92:95], v174 offset:1600
	v_cvt_pk_bf16_f32 v84, v96, v97
	v_cvt_pk_bf16_f32 v85, v98, v99
	v_cvt_pk_bf16_f32 v86, v100, v101
	v_cvt_pk_bf16_f32 v87, v102, v103
	s_waitcnt lgkmcnt(1)
	s_nop 0
	v_mfma_f32_32x32x16_bf16 v[66:81], v[88:91], v[84:87], v[66:81]
	s_waitcnt lgkmcnt(0)
	v_mfma_f32_32x32x16_bf16 v[50:65], v[92:95], v[84:87], v[50:65]
	ds_read_b128 v[88:91], v175 offset:1120
	ds_read_b128 v[92:95], v174 offset:1632
	v_cvt_pk_bf16_f32 v84, v106, v107
	v_cvt_pk_bf16_f32 v85, v110, v111
	v_cvt_pk_bf16_f32 v86, v168, v169
	v_cvt_pk_bf16_f32 v87, v172, v173
	s_waitcnt lgkmcnt(1)
	s_nop 0
	v_mfma_f32_32x32x16_bf16 v[66:81], v[88:91], v[84:87], v[66:81]
	s_waitcnt lgkmcnt(0)
	v_mfma_f32_32x32x16_bf16 v[50:65], v[92:95], v[84:87], v[50:65]
	ds_read_b128 v[168:171], v176 offset:6656
	ds_read_b128 v[82:85], v176
	ds_read_b128 v[172:175], v176 offset:32
	s_waitcnt lgkmcnt(1)
	v_mfma_f32_32x32x16_bf16 v[98:113], v[82:85], v[144:147], v[2:17]
	v_mfma_f32_32x32x16_bf16 v[82:97], v[168:171], v[144:147], v[2:17]
	ds_read_b128 v[168:171], v176 offset:6688
	s_waitcnt lgkmcnt(1)
	v_mfma_f32_32x32x16_bf16 v[98:113], v[172:175], v[140:143], v[98:113]
	s_waitcnt lgkmcnt(0)
	v_mfma_f32_32x32x16_bf16 v[82:97], v[168:171], v[140:143], v[82:97]
	ds_read_b128 v[168:171], v176 offset:64
	ds_read_b128 v[172:175], v176 offset:6720
	s_waitcnt lgkmcnt(1)
	v_mfma_f32_32x32x16_bf16 v[98:113], v[168:171], v[136:139], v[98:113]
	s_waitcnt lgkmcnt(0)
	v_mfma_f32_32x32x16_bf16 v[82:97], v[172:175], v[136:139], v[82:97]
	ds_read_b128 v[168:171], v176 offset:96
	ds_read_b128 v[172:175], v176 offset:6752
	s_waitcnt lgkmcnt(1)
	v_mfma_f32_32x32x16_bf16 v[98:113], v[168:171], v[132:135], v[98:113]
	s_waitcnt lgkmcnt(0)
	v_mfma_f32_32x32x16_bf16 v[82:97], v[172:175], v[132:135], v[82:97]
	ds_read_b128 v[168:171], v176 offset:128
	ds_read_b128 v[172:175], v176 offset:6784
	s_waitcnt lgkmcnt(1)
	v_mfma_f32_32x32x16_bf16 v[98:113], v[168:171], v[128:131], v[98:113]
	s_waitcnt lgkmcnt(0)
	v_mfma_f32_32x32x16_bf16 v[82:97], v[172:175], v[128:131], v[82:97]
	ds_read_b128 v[168:171], v176 offset:160
	ds_read_b128 v[172:175], v176 offset:6816
	s_waitcnt lgkmcnt(1)
	v_mfma_f32_32x32x16_bf16 v[98:113], v[168:171], v[124:127], v[98:113]
	v_lshl_add_u32 v168, s21, 6, v150
	v_cmp_le_i32_e32 vcc, v168, v151
	v_add_u32_e32 v169, 32, v168
	s_waitcnt lgkmcnt(0)
	v_mfma_f32_32x32x16_bf16 v[82:97], v[172:175], v[124:127], v[82:97]
	s_nop 6
	v_cndmask_b32_e32 v98, v232, v98, vcc
	v_cmp_le_i32_e32 vcc, v169, v151
	s_nop 2
	v_cndmask_b32_e32 v169, v232, v82, vcc
	v_or_b32_e32 v82, 1, v168
	v_cmp_le_i32_e32 vcc, v82, v151
	v_add_u32_e32 v82, 33, v168
	s_nop 0
	v_cndmask_b32_e32 v99, v232, v99, vcc
	v_cmp_le_i32_e32 vcc, v82, v151
	v_or_b32_e32 v82, 2, v168
	s_nop 0
	v_cndmask_b32_e32 v170, v232, v83, vcc
	v_cmp_le_i32_e32 vcc, v82, v151
	v_add_u32_e32 v82, 34, v168
	v_exp_f32_e32 v83, v99
	v_cndmask_b32_e32 v100, v232, v100, vcc
	v_cmp_le_i32_e32 vcc, v82, v151
	v_or_b32_e32 v82, 3, v168
	s_nop 0
	v_cndmask_b32_e32 v171, v232, v84, vcc
	v_cmp_le_i32_e32 vcc, v82, v151
	v_add_u32_e32 v82, 35, v168
	v_exp_f32_e32 v84, v100
	v_cndmask_b32_e32 v101, v232, v101, vcc
	v_cmp_le_i32_e32 vcc, v82, v151
	v_add_u32_e32 v82, 8, v168
	s_nop 0
	v_cndmask_b32_e32 v172, v232, v85, vcc
	v_cmp_le_i32_e32 vcc, v82, v151
	v_add_u32_e32 v82, 40, v168
	v_exp_f32_e32 v85, v101
	v_cndmask_b32_e32 v102, v232, v102, vcc
	v_cmp_le_i32_e32 vcc, v82, v151
	v_add_u32_e32 v82, 9, v168
	v_exp_f32_e32 v99, v172
	v_cndmask_b32_e32 v86, v232, v86, vcc
	v_cmp_le_i32_e32 vcc, v82, v151
	v_add_u32_e32 v82, 41, v168
	v_exp_f32_e32 v100, v86
	v_cndmask_b32_e32 v103, v232, v103, vcc
	v_cmp_le_i32_e32 vcc, v82, v151
	v_add_u32_e32 v82, 10, v168
	s_nop 0
	v_cndmask_b32_e32 v87, v232, v87, vcc
	v_cmp_le_i32_e32 vcc, v82, v151
	v_add_u32_e32 v82, 42, v168
	v_exp_f32_e32 v101, v87
	v_cndmask_b32_e32 v104, v232, v104, vcc
	v_cmp_le_i32_e32 vcc, v82, v151
	v_add_u32_e32 v82, 11, v168
	s_nop 0
	v_cndmask_b32_e32 v88, v232, v88, vcc
	v_cmp_le_i32_e32 vcc, v82, v151
	v_add_u32_e32 v82, 43, v168
	s_nop 0
	v_cndmask_b32_e32 v105, v232, v105, vcc
	v_cmp_le_i32_e32 vcc, v82, v151
	v_add_u32_e32 v82, 16, v168
	s_nop 0
	v_cndmask_b32_e32 v89, v232, v89, vcc
	v_cmp_le_i32_e32 vcc, v82, v151
	v_add_u32_e32 v82, 48, v168
	s_nop 0
	v_cndmask_b32_e32 v106, v232, v106, vcc
	v_cmp_le_i32_e32 vcc, v82, v151
	v_add_u32_e32 v82, 17, v168
	s_nop 0
	v_cndmask_b32_e32 v90, v232, v90, vcc
	v_cmp_le_i32_e32 vcc, v82, v151
	v_add_u32_e32 v82, 49, v168
	s_nop 0
	v_cndmask_b32_e32 v107, v232, v107, vcc
	v_cmp_le_i32_e32 vcc, v82, v151
	v_add_u32_e32 v82, 18, v168
	s_nop 0
	v_cndmask_b32_e32 v91, v232, v91, vcc
	v_cmp_le_i32_e32 vcc, v82, v151
	v_add_u32_e32 v82, 50, v168
	s_nop 0
	v_cndmask_b32_e32 v108, v232, v108, vcc
	v_cmp_le_i32_e32 vcc, v82, v151
	v_add_u32_e32 v82, 19, v168
	s_nop 0
	v_cndmask_b32_e32 v92, v232, v92, vcc
	v_cmp_le_i32_e32 vcc, v82, v151
	v_add_u32_e32 v82, 51, v168
	s_nop 0
	v_cndmask_b32_e32 v109, v232, v109, vcc
	v_cmp_le_i32_e32 vcc, v82, v151
	v_add_u32_e32 v82, 24, v168
	s_nop 0
	v_cndmask_b32_e32 v93, v232, v93, vcc
	v_cmp_le_i32_e32 vcc, v82, v151
	v_add_u32_e32 v82, 56, v168
	s_nop 0
	v_cndmask_b32_e32 v110, v232, v110, vcc
	v_cmp_le_i32_e32 vcc, v82, v151
	v_add_u32_e32 v82, 25, v168
	s_nop 0
	v_cndmask_b32_e32 v94, v232, v94, vcc
	v_cmp_le_i32_e32 vcc, v82, v151
	v_add_u32_e32 v82, 57, v168
	s_nop 0
	v_cndmask_b32_e32 v111, v232, v111, vcc
	v_cmp_le_i32_e32 vcc, v82, v151
	v_add_u32_e32 v82, 26, v168
	s_nop 0
	v_cndmask_b32_e32 v95, v232, v95, vcc
	v_cmp_le_i32_e32 vcc, v82, v151
	v_add_u32_e32 v82, 58, v168
	s_nop 0
	v_cndmask_b32_e32 v173, v232, v112, vcc
	v_cmp_le_i32_e32 vcc, v82, v151
	v_add_u32_e32 v82, 27, v168
	v_exp_f32_e32 v112, v102
	v_cndmask_b32_e32 v174, v232, v96, vcc
	v_cmp_le_i32_e32 vcc, v82, v151
	v_add_u32_e32 v82, 59, v168
	v_exp_f32_e32 v96, v169
	v_cndmask_b32_e32 v175, v232, v113, vcc
	v_cmp_le_i32_e32 vcc, v82, v151
	v_exp_f32_e32 v82, v98
	v_exp_f32_e32 v98, v171
	v_cndmask_b32_e32 v176, v232, v97, vcc
	v_exp_f32_e32 v97, v170
	v_exp_f32_e32 v113, v103
	v_pk_add_f32 v[86:87], v[164:165], v[82:83]
	v_exp_f32_e32 v168, v104
	v_pk_add_f32 v[86:87], v[96:97], v[86:87]
	v_exp_f32_e32 v169, v105
	v_pk_add_f32 v[86:87], v[84:85], v[86:87]
	v_cvt_pk_bf16_f32 v82, v82, v83
	v_pk_add_f32 v[86:87], v[98:99], v[86:87]
	v_cvt_pk_bf16_f32 v83, v84, v85
	v_pk_add_f32 v[86:87], v[112:113], v[86:87]
	v_cvt_pk_bf16_f32 v84, v112, v113
	v_add3_u32 v112, s20, v167, v160
	v_add_u32_e32 v112, v112, v160
	v_pk_add_f32 v[86:87], v[100:101], v[86:87]
	v_add_u32_e32 v113, 0x4000, v112
	v_pk_add_f32 v[86:87], v[168:169], v[86:87]
	v_cvt_pk_bf16_f32 v85, v168, v169
	ds_read_b128 v[168:171], v113 offset:1536
	v_exp_f32_e32 v102, v88
	v_exp_f32_e32 v103, v89
	v_exp_f32_e32 v104, v106
	v_exp_f32_e32 v105, v107
	v_exp_f32_e32 v88, v90
	v_exp_f32_e32 v89, v91
	v_add_u32_e32 v112, 0x3000, v112
	v_exp_f32_e32 v106, v108
	v_exp_f32_e32 v90, v92
	v_exp_f32_e32 v107, v109
	v_exp_f32_e32 v91, v93
	v_exp_f32_e32 v108, v110
	v_exp_f32_e32 v92, v94
	v_exp_f32_e32 v109, v111
	v_exp_f32_e32 v93, v95
	v_exp_f32_e32 v110, v173
	v_exp_f32_e32 v94, v174
	v_exp_f32_e32 v111, v175
	v_exp_f32_e32 v95, v176
	ds_read_b128 v[172:175], v112 offset:1024
	ds_read_b128 v[176:179], v112 offset:1056
	v_pk_add_f32 v[86:87], v[102:103], v[86:87]
	s_waitcnt lgkmcnt(1)
	v_mfma_f32_32x32x16_bf16 v[66:81], v[172:175], v[82:85], v[66:81]
	v_add_f32_e64 v86, v104, v86
	v_add_f32_e64 v87, v105, v87
	s_mov_b64 s[20:21], 0
	v_add_f32_e64 v86, v88, v86
	v_add_f32_e64 v87, v89, v87
	v_pk_add_f32 v[86:87], v[106:107], v[86:87]
	s_nop 0
	v_pk_add_f32 v[86:87], v[90:91], v[86:87]
	v_mfma_f32_32x32x16_bf16 v[50:65], v[168:171], v[82:85], v[50:65]
	v_cvt_pk_bf16_f32 v82, v104, v105
	v_cvt_pk_bf16_f32 v83, v106, v107
	ds_read_b128 v[104:107], v113 offset:1568
	v_cvt_pk_bf16_f32 v84, v108, v109
	v_cvt_pk_bf16_f32 v85, v110, v111
	v_pk_add_f32 v[86:87], v[108:109], v[86:87]
	s_waitcnt lgkmcnt(1)
	v_mfma_f32_32x32x16_bf16 v[66:81], v[176:179], v[82:85], v[66:81]
	v_add_f32_e64 v86, v92, v86
	v_add_f32_e64 v87, v93, v87
	v_add_f32_e64 v86, v110, v86
	v_add_f32_e64 v87, v111, v87
	v_add_f32_e64 v86, v94, v86
	v_add_f32_e64 v87, v95, v87
	s_waitcnt lgkmcnt(0)
	v_mfma_f32_32x32x16_bf16 v[50:65], v[104:107], v[82:85], v[50:65]
	v_cvt_pk_bf16_f32 v82, v96, v97
	v_cvt_pk_bf16_f32 v83, v98, v99
	v_cvt_pk_bf16_f32 v84, v100, v101
	v_cvt_pk_bf16_f32 v85, v102, v103
	ds_read_b128 v[96:99], v112 offset:1088
	ds_read_b128 v[100:103], v113 offset:1600
	s_waitcnt lgkmcnt(1)
	v_mfma_f32_32x32x16_bf16 v[66:81], v[96:99], v[82:85], v[66:81]
	s_waitcnt lgkmcnt(0)
	v_mfma_f32_32x32x16_bf16 v[50:65], v[100:103], v[82:85], v[50:65]
	v_cvt_pk_bf16_f32 v82, v88, v89
	v_cvt_pk_bf16_f32 v83, v90, v91
	v_cvt_pk_bf16_f32 v84, v92, v93
	v_cvt_pk_bf16_f32 v85, v94, v95
	ds_read_b128 v[88:91], v112 offset:1120
	ds_read_b128 v[92:95], v113 offset:1632
	s_waitcnt lgkmcnt(1)
	v_mfma_f32_32x32x16_bf16 v[66:81], v[88:91], v[82:85], v[66:81]
	s_waitcnt lgkmcnt(0)
	v_mfma_f32_32x32x16_bf16 v[50:65], v[92:95], v[82:85], v[50:65]
.LBB0_512:
	s_andn2_b64 vcc, exec, s[20:21]
	s_cbranch_vccnz .LBB0_514
	s_nop 9
	ds_read_b128 v[50:53], v166
	ds_read_b128 v[82:85], v166 offset:6656
	v_lshl_add_u32 v86, s19, 7, v150
	v_cmp_le_i32_e32 vcc, v86, v151
	v_add_u32_e32 v87, 32, v86
	s_waitcnt lgkmcnt(1)
	v_mfma_f32_32x32x16_bf16 v[66:81], v[50:53], v[144:147], v[2:17]
	s_waitcnt lgkmcnt(0)
	v_mfma_f32_32x32x16_bf16 v[50:65], v[82:85], v[144:147], v[2:17]
	ds_read_b128 v[82:85], v166 offset:32
	s_waitcnt lgkmcnt(0)
	v_mfma_f32_32x32x16_bf16 v[66:81], v[82:85], v[140:143], v[66:81]
	ds_read_b128 v[82:85], v166 offset:6688
	s_waitcnt lgkmcnt(0)
	v_mfma_f32_32x32x16_bf16 v[50:65], v[82:85], v[140:143], v[50:65]
	ds_read_b128 v[82:85], v166 offset:64
	s_waitcnt lgkmcnt(0)
	v_mfma_f32_32x32x16_bf16 v[66:81], v[82:85], v[136:139], v[66:81]
	ds_read_b128 v[82:85], v166 offset:6720
	s_waitcnt lgkmcnt(0)
	v_mfma_f32_32x32x16_bf16 v[50:65], v[82:85], v[136:139], v[50:65]
	ds_read_b128 v[82:85], v166 offset:96
	s_waitcnt lgkmcnt(0)
	v_mfma_f32_32x32x16_bf16 v[66:81], v[82:85], v[132:135], v[66:81]
	ds_read_b128 v[82:85], v166 offset:6752
	s_waitcnt lgkmcnt(0)
	v_mfma_f32_32x32x16_bf16 v[50:65], v[82:85], v[132:135], v[50:65]
	ds_read_b128 v[82:85], v166 offset:128
	s_waitcnt lgkmcnt(0)
	v_mfma_f32_32x32x16_bf16 v[66:81], v[82:85], v[128:131], v[66:81]
	ds_read_b128 v[82:85], v166 offset:6784
	s_waitcnt lgkmcnt(0)
	v_mfma_f32_32x32x16_bf16 v[50:65], v[82:85], v[128:131], v[50:65]
	ds_read_b128 v[82:85], v166 offset:160
	s_waitcnt lgkmcnt(0)
	v_mfma_f32_32x32x16_bf16 v[66:81], v[82:85], v[124:127], v[66:81]
	ds_read_b128 v[82:85], v166 offset:6816
	s_waitcnt lgkmcnt(0)
	v_mfma_f32_32x32x16_bf16 v[50:65], v[82:85], v[124:127], v[50:65]
	s_nop 8
	v_cndmask_b32_e32 v66, v232, v66, vcc
	v_cmp_le_i32_e32 vcc, v87, v151
	v_or_b32_e32 v82, 1, v86
	s_nop 0
	v_cndmask_b32_e32 v50, v232, v50, vcc
	v_cmp_le_i32_e32 vcc, v82, v151
	v_add_u32_e32 v82, 33, v86
	s_nop 0
	v_cndmask_b32_e32 v67, v232, v67, vcc
	v_cmp_le_i32_e32 vcc, v82, v151
	v_or_b32_e32 v82, 2, v86
	s_nop 0
	v_cndmask_b32_e32 v51, v232, v51, vcc
	v_cmp_le_i32_e32 vcc, v82, v151
	v_add_u32_e32 v82, 34, v86
	s_nop 0
	v_cndmask_b32_e32 v68, v232, v68, vcc
	v_cmp_le_i32_e32 vcc, v82, v151
	s_nop 1
	v_cndmask_b32_e32 v82, v232, v52, vcc
	v_or_b32_e32 v52, 3, v86
	v_cmp_le_i32_e32 vcc, v52, v151
	v_add_u32_e32 v52, 35, v86
	s_nop 0
	v_cndmask_b32_e32 v69, v232, v69, vcc
	v_cmp_le_i32_e32 vcc, v52, v151
	v_add_u32_e32 v52, 8, v86
	s_nop 0
	v_cndmask_b32_e32 v83, v232, v53, vcc
	v_cmp_le_i32_e32 vcc, v52, v151
	v_add_u32_e32 v52, 40, v86
	v_exp_f32_e32 v53, v51
	v_cndmask_b32_e32 v70, v232, v70, vcc
	v_cmp_le_i32_e32 vcc, v52, v151
	v_add_u32_e32 v52, 9, v86
	v_mul_u32_u24_e32 v51, 0x90, v193
	v_cndmask_b32_e32 v84, v232, v54, vcc
	v_cmp_le_i32_e32 vcc, v52, v151
	v_add_u32_e32 v52, 41, v86
	v_exp_f32_e32 v54, v82
	v_cndmask_b32_e32 v71, v232, v71, vcc
	v_cmp_le_i32_e32 vcc, v52, v151
	v_add_u32_e32 v52, 10, v86
	s_nop 0
	v_cndmask_b32_e32 v85, v232, v55, vcc
	v_cmp_le_i32_e32 vcc, v52, v151
	v_add_u32_e32 v52, 42, v86
	v_exp_f32_e32 v55, v83
	v_cndmask_b32_e32 v72, v232, v72, vcc
	v_cmp_le_i32_e32 vcc, v52, v151
	v_add_u32_e32 v52, 11, v86
	s_nop 0
	v_cndmask_b32_e32 v87, v232, v56, vcc
	v_cmp_le_i32_e32 vcc, v52, v151
	v_add_u32_e32 v52, 43, v86
	v_exp_f32_e32 v56, v68
	v_cndmask_b32_e32 v73, v232, v73, vcc
	v_cmp_le_i32_e32 vcc, v52, v151
	v_add_u32_e32 v52, 16, v86
	s_nop 0
	v_cndmask_b32_e32 v88, v232, v57, vcc
	v_cmp_le_i32_e32 vcc, v52, v151
	v_add_u32_e32 v52, 48, v86
	v_exp_f32_e32 v57, v69
	v_cndmask_b32_e32 v74, v232, v74, vcc
	v_cmp_le_i32_e32 vcc, v52, v151
	v_add_u32_e32 v52, 17, v86
	v_cvt_pk_bf16_f32 v69, v56, v57
	v_cndmask_b32_e32 v89, v232, v58, vcc
	v_cmp_le_i32_e32 vcc, v52, v151
	v_add_u32_e32 v52, 49, v86
	v_exp_f32_e32 v58, v84
	v_cndmask_b32_e32 v90, v232, v75, vcc
	v_cmp_le_i32_e32 vcc, v52, v151
	v_add_u32_e32 v52, 18, v86
	s_nop 0
	v_cndmask_b32_e32 v91, v232, v59, vcc
	v_cmp_le_i32_e32 vcc, v52, v151
	v_add_u32_e32 v52, 50, v86
	v_exp_f32_e32 v59, v85
	v_cndmask_b32_e32 v92, v232, v76, vcc
	v_cmp_le_i32_e32 vcc, v52, v151
	v_add_u32_e32 v52, 19, v86
	v_exp_f32_e32 v76, v66
	v_cndmask_b32_e32 v93, v232, v60, vcc
	v_cmp_le_i32_e32 vcc, v52, v151
	v_add_u32_e32 v52, 51, v86
	v_exp_f32_e32 v60, v70
	v_cndmask_b32_e32 v94, v232, v77, vcc
	v_cmp_le_i32_e32 vcc, v52, v151
	v_add_u32_e32 v52, 24, v86
	v_exp_f32_e32 v77, v67
	v_cndmask_b32_e32 v95, v232, v61, vcc
	v_cmp_le_i32_e32 vcc, v52, v151
	v_add_u32_e32 v52, 56, v86
	v_exp_f32_e32 v61, v71
	v_cndmask_b32_e32 v96, v232, v78, vcc
	v_cmp_le_i32_e32 vcc, v52, v151
	v_add_u32_e32 v52, 25, v86
	v_exp_f32_e32 v78, v74
	v_cndmask_b32_e32 v97, v232, v62, vcc
	v_cmp_le_i32_e32 vcc, v52, v151
	v_add_u32_e32 v52, 57, v86
	v_exp_f32_e32 v62, v72
	v_cndmask_b32_e32 v98, v232, v79, vcc
	v_cmp_le_i32_e32 vcc, v52, v151
	v_add_u32_e32 v52, 26, v86
	v_add3_u32 v72, s22, v51, v160
	v_add_u32_e32 v72, v72, v160
	v_cndmask_b32_e32 v99, v232, v63, vcc
	v_cmp_le_i32_e32 vcc, v52, v151
	v_add_u32_e32 v52, 58, v86
	v_add_u32_e32 v103, 0x3000, v72
	v_cndmask_b32_e32 v100, v232, v80, vcc
	v_cmp_le_i32_e32 vcc, v52, v151
	v_add_u32_e32 v52, 27, v86
	v_add_u32_e32 v104, 0x4000, v72
	v_cndmask_b32_e32 v101, v232, v64, vcc
	v_cmp_le_i32_e32 vcc, v52, v151
	v_add_u32_e32 v52, 59, v86
	v_exp_f32_e32 v63, v73
	v_cndmask_b32_e32 v81, v232, v81, vcc
	v_cmp_le_i32_e32 vcc, v52, v151
	ds_read_b128 v[72:75], v104 offset:1536
	v_cvt_pk_bf16_f32 v68, v76, v77
	v_cndmask_b32_e32 v102, v232, v65, vcc
	ds_read_b128 v[64:67], v103 offset:1024
	v_cvt_pk_bf16_f32 v70, v60, v61
	v_cvt_pk_bf16_f32 v71, v62, v63
	v_exp_f32_e32 v52, v50
	v_exp_f32_e32 v50, v87
	s_waitcnt lgkmcnt(0)
	v_mfma_f32_32x32x16_bf16 v[18:33], v[64:67], v[68:71], v[18:33]
	ds_read_b128 v[64:67], v103 offset:1056
	v_exp_f32_e32 v79, v90
	v_exp_f32_e32 v82, v92
	v_exp_f32_e32 v83, v94
	v_exp_f32_e32 v84, v96
	v_exp_f32_e32 v85, v98
	v_exp_f32_e32 v86, v100
	v_mfma_f32_32x32x16_bf16 v[34:49], v[72:75], v[68:71], v[34:49]
	ds_read_b128 v[72:75], v104 offset:1568
	v_exp_f32_e32 v87, v81
	v_cvt_pk_bf16_f32 v68, v78, v79
	v_cvt_pk_bf16_f32 v69, v82, v83
	v_cvt_pk_bf16_f32 v70, v84, v85
	v_cvt_pk_bf16_f32 v71, v86, v87
	v_pk_add_f32 v[76:77], v[162:163], v[76:77]
	v_exp_f32_e32 v51, v88
	s_waitcnt lgkmcnt(1)
	v_mfma_f32_32x32x16_bf16 v[18:33], v[64:67], v[68:71], v[18:33]
	ds_read_b128 v[64:67], v103 offset:1088
	v_exp_f32_e32 v80, v89
	v_exp_f32_e32 v81, v91
	v_exp_f32_e32 v88, v93
	v_exp_f32_e32 v89, v95
	v_exp_f32_e32 v90, v97
	v_exp_f32_e32 v91, v99
	s_waitcnt lgkmcnt(1)
	v_mfma_f32_32x32x16_bf16 v[34:49], v[72:75], v[68:71], v[34:49]
	ds_read_b128 v[72:75], v104 offset:1600
	v_cvt_pk_bf16_f32 v68, v52, v53
	v_add_f32_e64 v52, v52, v76
	v_add_f32_e64 v53, v53, v77
	v_cvt_pk_bf16_f32 v69, v54, v55
	v_pk_add_f32 v[52:53], v[56:57], v[52:53]
	v_cvt_pk_bf16_f32 v70, v58, v59
	v_pk_add_f32 v[52:53], v[54:55], v[52:53]
	v_cvt_pk_bf16_f32 v71, v50, v51
	v_pk_add_f32 v[52:53], v[60:61], v[52:53]
	v_exp_f32_e32 v92, v101
	v_pk_add_f32 v[52:53], v[58:59], v[52:53]
	s_waitcnt lgkmcnt(1)
	v_mfma_f32_32x32x16_bf16 v[18:33], v[64:67], v[68:71], v[18:33]
	v_add_f32_e64 v56, v62, v52
	v_add_f32_e64 v57, v63, v53
	ds_read_b128 v[52:55], v103 offset:1120
	ds_read_b128 v[60:63], v104 offset:1632
	v_exp_f32_e32 v93, v102
	v_pk_add_f32 v[50:51], v[50:51], v[56:57]
	v_cvt_pk_bf16_f32 v56, v80, v81
	v_cvt_pk_bf16_f32 v57, v88, v89
	s_waitcnt lgkmcnt(2)
	v_mfma_f32_32x32x16_bf16 v[34:49], v[72:75], v[68:71], v[34:49]
	v_cvt_pk_bf16_f32 v58, v90, v91
	v_cvt_pk_bf16_f32 v59, v92, v93
	v_add_f32_e64 v50, v78, v50
	v_add_f32_e64 v51, v79, v51
	v_add_f32_e64 v50, v80, v50
	v_add_f32_e64 v51, v81, v51
	v_pk_add_f32 v[50:51], v[82:83], v[50:51]
	s_waitcnt lgkmcnt(1)
	v_mfma_f32_32x32x16_bf16 v[18:33], v[52:55], v[56:59], v[18:33]
	v_add_f32_e64 v50, v88, v50
	v_add_f32_e64 v51, v89, v51
	v_add_f32_e64 v50, v84, v50
	v_add_f32_e64 v51, v85, v51
	v_add_f32_e64 v50, v90, v50
	v_add_f32_e64 v51, v91, v51
	s_nop 5
	v_mov_b64_e32 v[80:81], v[32:33]
	s_waitcnt lgkmcnt(0)
	v_mfma_f32_32x32x16_bf16 v[34:49], v[60:63], v[56:59], v[34:49]
	v_add_f32_e64 v50, v86, v50
	v_add_f32_e64 v51, v87, v51
	v_mov_b64_e32 v[78:79], v[30:31]
	v_add_f32_e64 v86, v92, v50
	v_add_f32_e64 v87, v93, v51
	v_mov_b64_e32 v[76:77], v[28:29]
	v_mov_b64_e32 v[74:75], v[26:27]
	v_mov_b64_e32 v[72:73], v[24:25]
	v_mov_b64_e32 v[70:71], v[22:23]
	s_nop 2
	v_mov_b64_e32 v[64:65], v[48:49]
	v_mov_b64_e32 v[62:63], v[46:47]
	v_mov_b64_e32 v[60:61], v[44:45]
	v_mov_b64_e32 v[58:59], v[42:43]
	v_mov_b64_e32 v[56:57], v[40:41]
	v_mov_b64_e32 v[54:55], v[38:39]
	v_mov_b64_e32 v[52:53], v[36:37]
	v_mov_b64_e32 v[50:51], v[34:35]
	v_mov_b64_e32 v[68:69], v[20:21]
	v_mov_b64_e32 v[66:67], v[18:19]

.LBB0_519:
	s_or_b64 exec, exec, s[22:23]
	global_load_dwordx4 v[30:33], v[30:31], off offset:128
	s_bitcmp1_b32 s25, 0
	s_cselect_b32 s22, 0xb000, 0
	s_add_i32 s25, s22, 0
	v_add_u32_e32 v34, s25, v188
	s_waitcnt vmcnt(3)
	ds_write_b128 v34, v[18:21]
	v_add_u32_e32 v18, s25, v189
	s_and_saveexec_b64 s[22:23], s[0:1]
	s_xor_b64 s[22:23], exec, s[22:23]
	s_cbranch_execz .LBB0_521
	s_waitcnt vmcnt(2)
	ds_write_b64 v18, v[22:23] offset:13312
	ds_write_b64 v18, v[24:25] offset:13328
	s_waitcnt vmcnt(1)
	ds_write_b128 v34, v[26:29] offset:22528
.LBB0_521:
	s_andn2_saveexec_b64 s[22:23], s[22:23]
	s_cbranch_execz .LBB0_523
	v_lshlrev_b32_e32 v19, 4, v191
	v_add3_u32 v19, v19, v192, s25
	ds_write_b128 v19, v[116:119]
	s_waitcnt vmcnt(2)
	ds_write_b64 v18, v[22:23] offset:13312
	ds_write_b64 v18, v[24:25] offset:13328
	s_waitcnt vmcnt(1)
	ds_write_b128 v34, v[26:29] offset:22528
	ds_write_b128 v19, v[120:123] offset:22528
.LBB0_523:
	s_or_b64 exec, exec, s[22:23]
	s_waitcnt vmcnt(0)
	ds_write_b64 v18, v[30:31] offset:35840
	ds_write_b64 v18, v[32:33] offset:35856

.LBB0_526:
	s_or_b64 exec, exec, s[22:23]
	s_waitcnt vmcnt(0)
	ds_write_b64 v26, v[30:31] offset:35840
	ds_write_b64 v26, v[32:33] offset:35856

.LBB0_533:
	s_or_b64 exec, exec, s[22:23]
	global_load_dwordx4 v[30:33], v[30:31], off offset:128
	s_bitcmp1_b32 s19, 0
	s_cselect_b32 s22, 0xb000, 0
	s_add_i32 s27, s22, 0
	v_add_u32_e32 v36, s27, v188
	s_waitcnt vmcnt(3)
	ds_write_b128 v36, v[26:29]
	v_add_u32_e32 v26, s27, v189
	s_and_saveexec_b64 s[22:23], s[0:1]
	s_xor_b64 s[22:23], exec, s[22:23]
	s_cbranch_execz .LBB0_535
	s_waitcnt vmcnt(2)
	ds_write_b64 v26, v[18:19] offset:13312
	ds_write_b64 v26, v[20:21] offset:13328
	s_waitcnt vmcnt(1)
	ds_write_b128 v36, v[22:25] offset:22528
.LBB0_535:
	s_andn2_saveexec_b64 s[22:23], s[22:23]
	s_cbranch_execz .LBB0_526
	v_add_u32_e32 v27, s27, v190
	ds_write_b128 v27, v[116:119]
	s_waitcnt vmcnt(2)
	ds_write_b64 v26, v[18:19] offset:13312
	ds_write_b64 v26, v[20:21] offset:13328
	s_waitcnt vmcnt(1)
	ds_write_b128 v36, v[22:25] offset:22528
	ds_write_b128 v27, v[120:123] offset:22528
	s_branch .LBB0_526

.LBB0_541:
	s_or_b64 exec, exec, s[14:15]
	global_load_dwordx4 v[30:33], v[148:149], off offset:128
	s_movk_i32 s14, 0xd0
	v_mul_lo_u32 v35, v161, s14
	v_lshl_add_u32 v188, v37, 4, v35
	v_add_u32_e32 v35, 0, v188
	v_mul_lo_u32 v192, v187, s14
	s_waitcnt vmcnt(3)
	ds_write_b128 v35, v[18:21]
	s_and_saveexec_b64 s[14:15], s[38:39]
	v_lshlrev_b32_e32 v18, 4, v191
	v_add3_u32 v18, 0, v18, v192
	ds_write_b128 v18, v[116:119]
	s_or_b64 exec, exec, s[14:15]
	s_movk_i32 s14, 0x90
	v_mul_lo_u32 v18, v34, s14
	v_and_b32_e32 v189, 6, v194
	v_lshl_add_u32 v189, v189, 4, v18
	v_and_b32_e32 v18, 1, v194
	v_lshl_add_u32 v189, v18, 3, v189
	v_add_u32_e32 v18, 0, v189
	s_waitcnt vmcnt(2)
	ds_write_b64 v18, v[22:23] offset:13312
	ds_write_b64 v18, v[24:25] offset:13328
	s_waitcnt vmcnt(1)
	ds_write_b128 v35, v[26:29] offset:22528
	s_and_saveexec_b64 s[14:15], s[38:39]
	v_lshlrev_b32_e32 v19, 4, v191
	v_add3_u32 v19, 0, v19, v192
	ds_write_b128 v19, v[120:123] offset:22528
	s_or_b64 exec, exec, s[14:15]
	s_lshl_b32 s19, s3, 2
	s_ashr_i32 s3, s21, 1
	s_add_i32 s3, s3, s19
	s_ashr_i32 s3, s3, 1
	s_mov_b64 s[14:15], -1
	s_cmp_gt_i32 s3, 0
	v_mul_u32_u24_e32 v114, 0x68, v193
	s_waitcnt vmcnt(0)
	ds_write_b64 v18, v[30:31] offset:35840
	ds_write_b64 v18, v[32:33] offset:35856
	s_waitcnt lgkmcnt(0)
	s_barrier
	s_cbranch_scc1 .LBB0_547
	v_mul_u32_u24_e32 v50, 0x68, v193
	s_mov_b64 s[14:15], 0

.LBB0_549:
	s_or_b64 exec, exec, s[16:17]
	s_add_i32 s22, s22, 2
	s_cmp_lg_u32 s3, s23
	s_waitcnt vmcnt(0)
	ds_write_b64 v62, v[94:95] offset:35840
	ds_write_b64 v62, v[96:97] offset:35856
	v_add_f32_e32 v66, v66, v67
	v_add_f32_e32 v80, v80, v81
	v_add_f32_e32 v68, v68, v69
	v_add_f32_e32 v52, v52, v53
	v_add_f32_e32 v70, v70, v71
	v_add_f32_e32 v50, v50, v51
	v_add_f32_e32 v72, v72, v73
	v_add_f32_e32 v54, v54, v55
	v_add_f32_e32 v182, v182, v183
	v_add_f32_e32 v184, v184, v185
	v_add_f32_e32 v76, v76, v77
	v_add_f32_e32 v58, v58, v59
	v_add_f32_e32 v74, v74, v75
	v_add_f32_e32 v56, v56, v57
	v_add_f32_e32 v78, v78, v79
	v_add_f32_e32 v60, v60, v61
	v_add_f32_e32 v66, v66, v80
	v_add_f32_e32 v68, v68, v52
	v_add_f32_e32 v70, v70, v50
	v_add_f32_e32 v72, v72, v54
	v_add_f32_e32 v182, v182, v184
	v_add_f32_e32 v76, v76, v58
	v_add_f32_e32 v74, v74, v56
	v_add_f32_e32 v78, v78, v60
	v_add_f32_e32 v66, v66, v68
	v_add_f32_e32 v70, v70, v72
	v_add_f32_e32 v182, v182, v76
	v_add_f32_e32 v74, v74, v78
	v_add_f32_e32 v162, v162, v66
	v_add_f32_e32 v163, v163, v70
	v_add_f32_e32 v162, v162, v182
	v_add_f32_e32 v163, v163, v74
	s_waitcnt lgkmcnt(0)
	s_barrier
	s_cbranch_scc0 .LBB0_559

.LBB0_554:
	s_or_b64 exec, exec, s[16:17]
	s_and_b32 s15, s22, 2
	s_mulk_i32 s15, 0x5800
	v_add_u32_e32 v96, s15, v195
	v_lshlrev_b32_e32 v97, 1, v160
	v_add_u32_e32 v112, v96, v97
	ds_read_b128 v[50:53], v112
	ds_read_b128 v[100:103], v112 offset:32
	ds_read_b128 v[104:107], v112 offset:6656
	ds_read_b128 v[108:111], v112 offset:6688
	ds_read_b128 v[164:167], v112 offset:64
	ds_read_b128 v[168:171], v112 offset:96
	ds_read_b128 v[176:179], v112 offset:6720
	ds_read_b128 v[198:201], v112 offset:6752
	ds_read_b128 v[202:205], v112 offset:128
	v_add_u32_e32 v96, v96, v197
	s_waitcnt lgkmcnt(8)
	v_mfma_f32_32x32x16_bf16 v[66:81], v[50:53], v[144:147], v[2:17]
	v_lshl_add_u32 v206, v150, 2, v96
	v_add_u32_e32 v175, 0x3000, v206
	v_add_u32_e32 v182, 0x4000, v206
	v_add3_u32 v207, v96, v196, v97
	v_add_u32_e32 v211, 0x9800, v206
	v_add_u32_e32 v210, 0x8800, v206
	s_add_i32 s23, s23, 1
	s_waitcnt lgkmcnt(7)
	v_mfma_f32_32x32x16_bf16 v[66:81], v[100:103], v[140:143], v[66:81]
	s_bitcmp1_b32 s23, 0
	s_cselect_b32 s15, 0xb000, 0
	s_add_i32 s15, s15, 0
	s_waitcnt lgkmcnt(6)
	v_mfma_f32_32x32x16_bf16 v[50:65], v[104:107], v[144:147], v[2:17]
	ds_read_b128 v[100:103], v112 offset:160
	s_waitcnt lgkmcnt(5)
	v_mfma_f32_32x32x16_bf16 v[66:81], v[164:167], v[136:139], v[66:81]
	v_mfma_f32_32x32x16_bf16 v[50:65], v[108:111], v[140:143], v[50:65]
	ds_read_b128 v[104:107], v112 offset:6784
	s_waitcnt lgkmcnt(5)
	v_mfma_f32_32x32x16_bf16 v[66:81], v[168:171], v[132:135], v[66:81]
	ds_read_b128 v[108:111], v112 offset:6816
	s_waitcnt lgkmcnt(5)
	v_mfma_f32_32x32x16_bf16 v[50:65], v[176:179], v[136:139], v[50:65]
	s_waitcnt lgkmcnt(3)
	v_mfma_f32_32x32x16_bf16 v[66:81], v[202:205], v[128:131], v[66:81]
	v_mfma_f32_32x32x16_bf16 v[50:65], v[198:201], v[132:135], v[50:65]
	s_waitcnt lgkmcnt(2)
	v_mfma_f32_32x32x16_bf16 v[66:81], v[100:103], v[124:127], v[66:81]
	s_waitcnt lgkmcnt(1)
	v_mfma_f32_32x32x16_bf16 v[50:65], v[104:107], v[128:131], v[50:65]
	s_nop 9
	v_exp_f32_e32 v100, v66
	v_exp_f32_e32 v101, v67
	v_exp_f32_e32 v102, v68
	v_exp_f32_e32 v103, v69
	ds_read_b128 v[66:69], v175 offset:1024
	v_exp_f32_e32 v104, v70
	v_exp_f32_e32 v105, v71
	v_exp_f32_e32 v106, v72
	v_exp_f32_e32 v107, v73
	v_cvt_pk_bf16_f32 v70, v100, v101
	v_cvt_pk_bf16_f32 v71, v102, v103
	v_cvt_pk_bf16_f32 v72, v104, v105
	v_cvt_pk_bf16_f32 v73, v106, v107
	s_waitcnt lgkmcnt(1)
	v_mfma_f32_32x32x16_bf16 v[50:65], v[108:111], v[124:127], v[50:65]
	v_exp_f32_e32 v112, v74
	v_exp_f32_e32 v113, v75
	v_exp_f32_e32 v110, v76
	v_exp_f32_e32 v111, v77
	ds_read_b128 v[74:77], v175 offset:1056
	v_exp_f32_e32 v108, v78
	v_exp_f32_e32 v109, v79
	s_waitcnt lgkmcnt(1)
	v_mfma_f32_32x32x16_bf16 v[18:33], v[66:69], v[70:73], v[18:33]
	ds_read_b128 v[66:69], v182 offset:1536
	v_exp_f32_e32 v164, v80
	v_exp_f32_e32 v165, v81
	v_exp_f32_e32 v170, v50
	v_exp_f32_e32 v171, v51
	v_exp_f32_e32 v168, v52
	v_exp_f32_e32 v169, v53
	s_waitcnt lgkmcnt(0)
	v_mfma_f32_32x32x16_bf16 v[34:49], v[66:69], v[70:73], v[34:49]
	v_cvt_pk_bf16_f32 v66, v112, v113
	v_cvt_pk_bf16_f32 v67, v110, v111
	v_cvt_pk_bf16_f32 v68, v108, v109
	v_cvt_pk_bf16_f32 v69, v164, v165
	ds_read_b128 v[50:53], v175 offset:1088
	ds_read_b128 v[70:73], v182 offset:1568
	v_exp_f32_e32 v166, v54
	v_mfma_f32_32x32x16_bf16 v[18:33], v[74:77], v[66:69], v[18:33]
	v_exp_f32_e32 v167, v55
	v_exp_f32_e32 v172, v56
	v_exp_f32_e32 v173, v57
	v_cvt_pk_bf16_f32 v54, v170, v171
	v_cvt_pk_bf16_f32 v55, v168, v169
	v_cvt_pk_bf16_f32 v56, v166, v167
	v_cvt_pk_bf16_f32 v57, v172, v173
	s_waitcnt lgkmcnt(0)
	v_mfma_f32_32x32x16_bf16 v[34:49], v[70:73], v[66:69], v[34:49]
	v_exp_f32_e32 v178, v58
	v_exp_f32_e32 v179, v59
	v_exp_f32_e32 v176, v60
	v_exp_f32_e32 v177, v61
	ds_read_b128 v[58:61], v175 offset:1120
	v_exp_f32_e32 v174, v62
	v_exp_f32_e32 v175, v63
	v_mfma_f32_32x32x16_bf16 v[18:33], v[50:53], v[54:57], v[18:33]
	ds_read_b128 v[50:53], v182 offset:1600
	v_exp_f32_e32 v180, v64
	v_exp_f32_e32 v181, v65
	s_waitcnt lgkmcnt(0)
	v_mfma_f32_32x32x16_bf16 v[34:49], v[50:53], v[54:57], v[34:49]
	ds_read_b128 v[54:57], v182 offset:1632
	v_cvt_pk_bf16_f32 v50, v178, v179
	v_cvt_pk_bf16_f32 v51, v176, v177
	v_cvt_pk_bf16_f32 v52, v174, v175
	v_cvt_pk_bf16_f32 v53, v180, v181
	s_nop 1
	v_mfma_f32_32x32x16_bf16 v[18:33], v[58:61], v[50:53], v[18:33]
	s_waitcnt lgkmcnt(0)
	v_mfma_f32_32x32x16_bf16 v[34:49], v[54:57], v[50:53], v[34:49]
	ds_read_b128 v[50:53], v207 offset:22528
	ds_read_b128 v[182:185], v207 offset:22560
	ds_read_b128 v[198:201], v207 offset:29184
	ds_read_b128 v[202:205], v207 offset:29216
	s_waitcnt lgkmcnt(3)
	v_mfma_f32_32x32x16_bf16 v[66:81], v[50:53], v[144:147], v[2:17]
	v_add_f32_e32 v100, v100, v101
	v_add_f32_e32 v170, v170, v171
	v_add_f32_e32 v102, v102, v103
	s_waitcnt lgkmcnt(1)
	v_mfma_f32_32x32x16_bf16 v[50:65], v[198:201], v[144:147], v[2:17]
	v_add_f32_e32 v168, v168, v169
	v_add_f32_e32 v104, v104, v105
	v_add_f32_e32 v166, v166, v167
	v_mfma_f32_32x32x16_bf16 v[66:81], v[182:185], v[140:143], v[66:81]
	v_add_f32_e32 v106, v106, v107
	v_add_f32_e32 v172, v172, v173
	v_add_f32_e32 v112, v112, v113
	ds_read_b128 v[182:185], v207 offset:22592
	ds_read_b128 v[198:201], v207 offset:22624
	s_waitcnt lgkmcnt(2)
	v_mfma_f32_32x32x16_bf16 v[50:65], v[202:205], v[140:143], v[50:65]
	v_add_f32_e32 v178, v178, v179
	v_add_f32_e32 v110, v110, v111
	v_add_f32_e32 v176, v176, v177
	s_waitcnt lgkmcnt(1)
	v_mfma_f32_32x32x16_bf16 v[66:81], v[182:185], v[136:139], v[66:81]
	v_add_f32_e32 v108, v108, v109
	v_add_f32_e32 v174, v174, v175
	v_add_f32_e32 v164, v164, v165
	ds_read_b128 v[182:185], v207 offset:29248
	ds_read_b128 v[202:205], v207 offset:29280
	s_waitcnt lgkmcnt(1)
	v_mfma_f32_32x32x16_bf16 v[50:65], v[182:185], v[136:139], v[50:65]
	v_add_f32_e32 v180, v180, v181
	v_add_f32_e32 v100, v100, v170
	v_add_f32_e32 v102, v102, v168
	v_mfma_f32_32x32x16_bf16 v[66:81], v[198:201], v[132:135], v[66:81]
	v_add_f32_e32 v104, v104, v166
	v_add_f32_e32 v106, v106, v172
	v_add_f32_e32 v112, v112, v178
	ds_read_b128 v[182:185], v207 offset:22656
	ds_read_b128 v[198:201], v207 offset:22688
	global_load_dwordx4 v[94:97], v[94:95], off offset:128
	s_waitcnt lgkmcnt(1)
	v_mfma_f32_32x32x16_bf16 v[66:81], v[182:185], v[128:131], v[66:81]
	v_add_f32_e32 v110, v110, v176
	v_add_f32_e32 v108, v108, v174
	ds_read_b128 v[182:185], v207 offset:29312
	v_mfma_f32_32x32x16_bf16 v[50:65], v[202:205], v[132:135], v[50:65]
	v_add_f32_e32 v164, v164, v180
	ds_read_b128 v[202:205], v211 offset:1536
	s_waitcnt lgkmcnt(2)
	v_mfma_f32_32x32x16_bf16 v[66:81], v[198:201], v[124:127], v[66:81]
	ds_read_b128 v[198:201], v207 offset:29344
	ds_read_b128 v[206:209], v210 offset:1056
	s_waitcnt lgkmcnt(3)
	v_mfma_f32_32x32x16_bf16 v[50:65], v[182:185], v[128:131], v[50:65]
	v_add_f32_e32 v100, v100, v102
	ds_read_b128 v[182:185], v210 offset:1024
	v_add_f32_e32 v104, v104, v106
	v_add_f32_e32 v112, v112, v110
	v_add_f32_e32 v108, v108, v164
	v_add_f32_e32 v162, v162, v100
	v_add_f32_e32 v163, v163, v104
	v_add_f32_e32 v162, v162, v112
	v_add_f32_e32 v163, v163, v108
	v_exp_f32_e32 v66, v66
	v_exp_f32_e32 v67, v67
	v_exp_f32_e32 v68, v68
	v_exp_f32_e32 v69, v69
	v_exp_f32_e32 v70, v70
	v_exp_f32_e32 v71, v71
	v_exp_f32_e32 v72, v72
	v_exp_f32_e32 v73, v73
	s_waitcnt lgkmcnt(2)
	v_mfma_f32_32x32x16_bf16 v[50:65], v[198:201], v[124:127], v[50:65]
	v_cvt_pk_bf16_f32 v198, v66, v67
	v_cvt_pk_bf16_f32 v199, v68, v69
	v_cvt_pk_bf16_f32 v200, v70, v71
	v_cvt_pk_bf16_f32 v201, v72, v73
	v_exp_f32_e32 v76, v76
	v_exp_f32_e32 v77, v77
	s_nop 5
	v_exp_f32_e32 v52, v52
	v_mfma_f32_32x32x16_bf16 v[34:49], v[202:205], v[198:201], v[34:49]
	ds_read_b128 v[202:205], v211 offset:1568
	v_exp_f32_e32 v53, v53
	s_waitcnt lgkmcnt(1)
	v_mfma_f32_32x32x16_bf16 v[18:33], v[182:185], v[198:201], v[18:33]
	v_exp_f32_e32 v182, v74
	v_exp_f32_e32 v183, v75
	v_exp_f32_e32 v74, v78
	v_exp_f32_e32 v75, v79
	v_exp_f32_e32 v78, v80
	v_exp_f32_e32 v79, v81
	v_cvt_pk_bf16_f32 v198, v182, v183
	v_cvt_pk_bf16_f32 v199, v76, v77
	v_cvt_pk_bf16_f32 v200, v74, v75
	v_cvt_pk_bf16_f32 v201, v78, v79
	v_exp_f32_e32 v80, v50
	v_exp_f32_e32 v81, v51
	v_mfma_f32_32x32x16_bf16 v[18:33], v[206:209], v[198:201], v[18:33]
	ds_read_b128 v[206:209], v210 offset:1088
	v_exp_f32_e32 v50, v54
	v_exp_f32_e32 v51, v55
	v_exp_f32_e32 v54, v56
	v_exp_f32_e32 v55, v57
	v_exp_f32_e32 v184, v58
	v_exp_f32_e32 v185, v59
	s_waitcnt lgkmcnt(1)
	v_mfma_f32_32x32x16_bf16 v[34:49], v[202:205], v[198:201], v[34:49]
	ds_read_b128 v[202:205], v211 offset:1600
	v_cvt_pk_bf16_f32 v198, v80, v81
	v_cvt_pk_bf16_f32 v199, v52, v53
	v_cvt_pk_bf16_f32 v200, v50, v51
	v_cvt_pk_bf16_f32 v201, v54, v55
	v_exp_f32_e32 v58, v60
	v_exp_f32_e32 v59, v61
	s_waitcnt lgkmcnt(1)
	v_mfma_f32_32x32x16_bf16 v[18:33], v[206:209], v[198:201], v[18:33]
	ds_read_b128 v[206:209], v210 offset:1120
	v_exp_f32_e32 v56, v62
	v_exp_f32_e32 v57, v63
	v_exp_f32_e32 v60, v64
	v_exp_f32_e32 v61, v65
	v_add_u32_e32 v63, s15, v188
	v_add_u32_e32 v62, s15, v189
	s_waitcnt lgkmcnt(1)
	v_mfma_f32_32x32x16_bf16 v[34:49], v[202:205], v[198:201], v[34:49]
	ds_read_b128 v[202:205], v211 offset:1632
	v_cvt_pk_bf16_f32 v198, v184, v185
	v_cvt_pk_bf16_f32 v199, v58, v59
	v_cvt_pk_bf16_f32 v200, v56, v57
	v_cvt_pk_bf16_f32 v201, v60, v61
	s_waitcnt vmcnt(3)
	ds_write_b128 v63, v[90:93]
	s_waitcnt lgkmcnt(2)
	v_mfma_f32_32x32x16_bf16 v[18:33], v[206:209], v[198:201], v[18:33]
	s_waitcnt lgkmcnt(1)
	v_mfma_f32_32x32x16_bf16 v[34:49], v[202:205], v[198:201], v[34:49]
	s_and_saveexec_b64 s[16:17], s[0:1]
	s_xor_b64 s[16:17], exec, s[16:17]
	s_cbranch_execz .LBB0_556
	s_waitcnt vmcnt(2)
	ds_write_b64 v62, v[82:83] offset:13312
	ds_write_b64 v62, v[84:85] offset:13328
	s_waitcnt vmcnt(1)
	ds_write_b128 v63, v[86:89] offset:22528
.LBB0_556:
	s_andn2_saveexec_b64 s[16:17], s[16:17]
	s_cbranch_execz .LBB0_549
	v_add_u32_e32 v64, s15, v190
	ds_write_b128 v64, v[116:119]
	s_waitcnt vmcnt(2)
	ds_write_b64 v62, v[82:83] offset:13312
	ds_write_b64 v62, v[84:85] offset:13328
	s_waitcnt vmcnt(1)
	ds_write_b128 v63, v[86:89] offset:22528
	ds_write_b128 v64, v[120:123] offset:22528
	s_branch .LBB0_549

.LBB0_560:
	s_lshl_b32 s17, s3, 1
	s_and_b32 s15, s17, 2
	s_mulk_i32 s15, 0x5800
	s_and_b32 s14, s21, 2
	s_add_i32 s16, s15, 0
	v_lshlrev_b32_e32 v82, 1, v50
	v_lshlrev_b32_e32 v83, 1, v160
	v_lshlrev_b32_e32 v114, 3, v194
	s_cmp_eq_u32 s14, 0
	v_add3_u32 v166, s16, v82, v83
	s_mov_b64 s[14:15], -1
	s_cbranch_scc1 .LBB0_562
	ds_read_b128 v[84:87], v166 offset:6656
	ds_read_b128 v[66:69], v166
	ds_read_b128 v[88:91], v166 offset:32
	s_or_b32 s15, s17, 1
	s_and_b32 s14, s15, 3
	s_mulk_i32 s14, 0x5800
	s_waitcnt lgkmcnt(1)
	v_mfma_f32_32x32x16_bf16 v[50:65], v[66:69], v[144:147], v[2:17]
	s_add_i32 s14, s14, 0
	v_add3_u32 v176, s14, v82, v83
	v_mfma_f32_32x32x16_bf16 v[66:81], v[84:87], v[144:147], v[2:17]
	ds_read_b128 v[84:87], v166 offset:6688
	s_waitcnt lgkmcnt(1)
	v_mfma_f32_32x32x16_bf16 v[50:65], v[88:91], v[140:143], v[50:65]
	s_waitcnt lgkmcnt(0)
	v_mfma_f32_32x32x16_bf16 v[66:81], v[84:87], v[140:143], v[66:81]
	ds_read_b128 v[84:87], v166 offset:64
	ds_read_b128 v[88:91], v166 offset:6720
	s_waitcnt lgkmcnt(1)
	v_mfma_f32_32x32x16_bf16 v[50:65], v[84:87], v[136:139], v[50:65]
	s_waitcnt lgkmcnt(0)
	v_mfma_f32_32x32x16_bf16 v[66:81], v[88:91], v[136:139], v[66:81]
	ds_read_b128 v[84:87], v166 offset:96
	ds_read_b128 v[88:91], v166 offset:6752
	s_waitcnt lgkmcnt(1)
	v_mfma_f32_32x32x16_bf16 v[50:65], v[84:87], v[132:135], v[50:65]
	s_waitcnt lgkmcnt(0)
	v_mfma_f32_32x32x16_bf16 v[66:81], v[88:91], v[132:135], v[66:81]
	ds_read_b128 v[84:87], v166 offset:128
	ds_read_b128 v[88:91], v166 offset:6784
	s_waitcnt lgkmcnt(1)
	v_mfma_f32_32x32x16_bf16 v[50:65], v[84:87], v[128:131], v[50:65]
	s_waitcnt lgkmcnt(0)
	v_mfma_f32_32x32x16_bf16 v[66:81], v[88:91], v[128:131], v[66:81]
	ds_read_b128 v[84:87], v166 offset:160
	ds_read_b128 v[88:91], v166 offset:6816
	s_waitcnt lgkmcnt(1)
	v_mfma_f32_32x32x16_bf16 v[50:65], v[84:87], v[124:127], v[50:65]
	s_waitcnt lgkmcnt(0)
	v_mfma_f32_32x32x16_bf16 v[66:81], v[88:91], v[124:127], v[66:81]
	s_nop 9
	v_exp_f32_e32 v50, v50
	v_exp_f32_e32 v51, v51
	v_exp_f32_e32 v52, v52
	v_exp_f32_e32 v53, v53
	v_exp_f32_e32 v54, v54
	v_exp_f32_e32 v55, v55
	v_exp_f32_e32 v104, v58
	v_exp_f32_e32 v96, v66
	v_exp_f32_e32 v97, v67
	v_exp_f32_e32 v98, v68
	v_exp_f32_e32 v99, v69
	v_exp_f32_e32 v105, v59
	v_pk_add_f32 v[58:59], v[162:163], v[50:51]
	v_exp_f32_e32 v100, v70
	v_exp_f32_e32 v101, v71
	v_pk_add_f32 v[58:59], v[96:97], v[58:59]
	v_exp_f32_e32 v56, v56
	v_exp_f32_e32 v57, v57
	v_pk_add_f32 v[58:59], v[52:53], v[58:59]
	v_cvt_pk_bf16_f32 v84, v50, v51
	v_mul_u32_u24_e32 v50, 0x48, v193
	v_exp_f32_e32 v102, v72
	v_exp_f32_e32 v103, v73
	v_pk_add_f32 v[58:59], v[98:99], v[58:59]
	v_lshlrev_b32_e32 v167, 1, v50
	v_pk_add_f32 v[58:59], v[54:55], v[58:59]
	v_add3_u32 v50, s16, v167, v160
	v_add_u32_e32 v50, v50, v160
	v_exp_f32_e32 v106, v74
	v_exp_f32_e32 v107, v75
	v_pk_add_f32 v[58:59], v[100:101], v[58:59]
	v_add_u32_e32 v174, 0x4000, v50
	v_exp_f32_e32 v108, v60
	v_exp_f32_e32 v109, v61
	v_pk_add_f32 v[58:59], v[56:57], v[58:59]
	ds_read_b128 v[88:91], v174 offset:1536
	v_exp_f32_e32 v110, v76
	v_exp_f32_e32 v111, v77
	v_pk_add_f32 v[58:59], v[102:103], v[58:59]
	v_exp_f32_e32 v112, v62
	v_exp_f32_e32 v113, v63
	v_pk_add_f32 v[58:59], v[104:105], v[58:59]
	v_exp_f32_e32 v168, v78
	v_exp_f32_e32 v169, v79
	v_pk_add_f32 v[58:59], v[106:107], v[58:59]
	v_exp_f32_e32 v170, v64
	v_exp_f32_e32 v171, v65
	v_pk_add_f32 v[58:59], v[108:109], v[58:59]
	v_add_u32_e32 v175, 0x3000, v50
	v_exp_f32_e32 v172, v80
	v_exp_f32_e32 v173, v81
	v_pk_add_f32 v[58:59], v[110:111], v[58:59]
	v_cvt_pk_bf16_f32 v85, v52, v53
	ds_read_b128 v[50:53], v175 offset:1024
	ds_read_b128 v[92:95], v175 offset:1056
	v_pk_add_f32 v[58:59], v[112:113], v[58:59]
	v_cvt_pk_bf16_f32 v86, v54, v55
	v_pk_add_f32 v[58:59], v[168:169], v[58:59]
	v_cvt_pk_bf16_f32 v87, v56, v57
	v_pk_add_f32 v[58:59], v[170:171], v[58:59]
	s_nop 0
	v_pk_add_f32 v[164:165], v[172:173], v[58:59]
	s_waitcnt lgkmcnt(1)
	v_mfma_f32_32x32x16_bf16 v[66:81], v[50:53], v[84:87], v[18:33]
	v_mfma_f32_32x32x16_bf16 v[50:65], v[88:91], v[84:87], v[34:49]
	ds_read_b128 v[88:91], v174 offset:1568
	v_cvt_pk_bf16_f32 v84, v104, v105
	v_cvt_pk_bf16_f32 v85, v108, v109
	v_cvt_pk_bf16_f32 v86, v112, v113
	v_cvt_pk_bf16_f32 v87, v170, v171
	s_waitcnt lgkmcnt(1)
	s_nop 0
	v_mfma_f32_32x32x16_bf16 v[66:81], v[92:95], v[84:87], v[66:81]
	s_waitcnt lgkmcnt(0)
	v_mfma_f32_32x32x16_bf16 v[50:65], v[88:91], v[84:87], v[50:65]
	ds_read_b128 v[88:91], v175 offset:1088
	ds_read_b128 v[92:95], v174 offset:1600
	v_cvt_pk_bf16_f32 v84, v96, v97
	v_cvt_pk_bf16_f32 v85, v98, v99
	v_cvt_pk_bf16_f32 v86, v100, v101
	v_cvt_pk_bf16_f32 v87, v102, v103
	s_waitcnt lgkmcnt(1)
	s_nop 0
	v_mfma_f32_32x32x16_bf16 v[66:81], v[88:91], v[84:87], v[66:81]
	s_waitcnt lgkmcnt(0)
	v_mfma_f32_32x32x16_bf16 v[50:65], v[92:95], v[84:87], v[50:65]
	ds_read_b128 v[88:91], v175 offset:1120
	ds_read_b128 v[92:95], v174 offset:1632
	v_cvt_pk_bf16_f32 v84, v106, v107
	v_cvt_pk_bf16_f32 v85, v110, v111
	v_cvt_pk_bf16_f32 v86, v168, v169
	v_cvt_pk_bf16_f32 v87, v172, v173
	s_waitcnt lgkmcnt(1)
	s_nop 0
	v_mfma_f32_32x32x16_bf16 v[66:81], v[88:91], v[84:87], v[66:81]
	s_waitcnt lgkmcnt(0)
	v_mfma_f32_32x32x16_bf16 v[50:65], v[92:95], v[84:87], v[50:65]
	ds_read_b128 v[168:171], v176 offset:6656
	ds_read_b128 v[82:85], v176
	ds_read_b128 v[172:175], v176 offset:32
	s_waitcnt lgkmcnt(1)
	v_mfma_f32_32x32x16_bf16 v[98:113], v[82:85], v[144:147], v[2:17]
	v_mfma_f32_32x32x16_bf16 v[82:97], v[168:171], v[144:147], v[2:17]
	ds_read_b128 v[168:171], v176 offset:6688
	s_waitcnt lgkmcnt(1)
	v_mfma_f32_32x32x16_bf16 v[98:113], v[172:175], v[140:143], v[98:113]
	s_waitcnt lgkmcnt(0)
	v_mfma_f32_32x32x16_bf16 v[82:97], v[168:171], v[140:143], v[82:97]
	ds_read_b128 v[168:171], v176 offset:64
	ds_read_b128 v[172:175], v176 offset:6720
	s_waitcnt lgkmcnt(1)
	v_mfma_f32_32x32x16_bf16 v[98:113], v[168:171], v[136:139], v[98:113]
	s_waitcnt lgkmcnt(0)
	v_mfma_f32_32x32x16_bf16 v[82:97], v[172:175], v[136:139], v[82:97]
	ds_read_b128 v[168:171], v176 offset:96
	ds_read_b128 v[172:175], v176 offset:6752
	s_waitcnt lgkmcnt(1)
	v_mfma_f32_32x32x16_bf16 v[98:113], v[168:171], v[132:135], v[98:113]
	s_waitcnt lgkmcnt(0)
	v_mfma_f32_32x32x16_bf16 v[82:97], v[172:175], v[132:135], v[82:97]
	ds_read_b128 v[168:171], v176 offset:128
	ds_read_b128 v[172:175], v176 offset:6784
	s_waitcnt lgkmcnt(1)
	v_mfma_f32_32x32x16_bf16 v[98:113], v[168:171], v[128:131], v[98:113]
	s_waitcnt lgkmcnt(0)
	v_mfma_f32_32x32x16_bf16 v[82:97], v[172:175], v[128:131], v[82:97]
	ds_read_b128 v[168:171], v176 offset:160
	ds_read_b128 v[172:175], v176 offset:6816
	s_waitcnt lgkmcnt(1)
	v_mfma_f32_32x32x16_bf16 v[98:113], v[168:171], v[124:127], v[98:113]
	v_lshl_add_u32 v168, s15, 6, v150
	v_cmp_le_i32_e32 vcc, v168, v151
	v_add_u32_e32 v169, 32, v168
	s_waitcnt lgkmcnt(0)
	v_mfma_f32_32x32x16_bf16 v[82:97], v[172:175], v[124:127], v[82:97]
	s_nop 6
	v_cndmask_b32_e32 v98, v232, v98, vcc
	v_cmp_le_i32_e32 vcc, v169, v151
	s_nop 2
	v_cndmask_b32_e32 v169, v232, v82, vcc
	v_or_b32_e32 v82, 1, v168
	v_cmp_le_i32_e32 vcc, v82, v151
	v_add_u32_e32 v82, 33, v168
	s_nop 0
	v_cndmask_b32_e32 v99, v232, v99, vcc
	v_cmp_le_i32_e32 vcc, v82, v151
	v_or_b32_e32 v82, 2, v168
	s_nop 0
	v_cndmask_b32_e32 v170, v232, v83, vcc
	v_cmp_le_i32_e32 vcc, v82, v151
	v_add_u32_e32 v82, 34, v168
	v_exp_f32_e32 v83, v99
	v_cndmask_b32_e32 v100, v232, v100, vcc
	v_cmp_le_i32_e32 vcc, v82, v151
	v_or_b32_e32 v82, 3, v168
	s_nop 0
	v_cndmask_b32_e32 v171, v232, v84, vcc
	v_cmp_le_i32_e32 vcc, v82, v151
	v_add_u32_e32 v82, 35, v168
	v_exp_f32_e32 v84, v100
	v_cndmask_b32_e32 v101, v232, v101, vcc
	v_cmp_le_i32_e32 vcc, v82, v151
	v_add_u32_e32 v82, 8, v168
	s_nop 0
	v_cndmask_b32_e32 v172, v232, v85, vcc
	v_cmp_le_i32_e32 vcc, v82, v151
	v_add_u32_e32 v82, 40, v168
	v_exp_f32_e32 v85, v101
	v_cndmask_b32_e32 v102, v232, v102, vcc
	v_cmp_le_i32_e32 vcc, v82, v151
	v_add_u32_e32 v82, 9, v168
	v_exp_f32_e32 v99, v172
	v_cndmask_b32_e32 v86, v232, v86, vcc
	v_cmp_le_i32_e32 vcc, v82, v151
	v_add_u32_e32 v82, 41, v168
	v_exp_f32_e32 v100, v86
	v_cndmask_b32_e32 v103, v232, v103, vcc
	v_cmp_le_i32_e32 vcc, v82, v151
	v_add_u32_e32 v82, 10, v168
	s_nop 0
	v_cndmask_b32_e32 v87, v232, v87, vcc
	v_cmp_le_i32_e32 vcc, v82, v151
	v_add_u32_e32 v82, 42, v168
	v_exp_f32_e32 v101, v87
	v_cndmask_b32_e32 v104, v232, v104, vcc
	v_cmp_le_i32_e32 vcc, v82, v151
	v_add_u32_e32 v82, 11, v168
	s_nop 0
	v_cndmask_b32_e32 v88, v232, v88, vcc
	v_cmp_le_i32_e32 vcc, v82, v151
	v_add_u32_e32 v82, 43, v168
	s_nop 0
	v_cndmask_b32_e32 v105, v232, v105, vcc
	v_cmp_le_i32_e32 vcc, v82, v151
	v_add_u32_e32 v82, 16, v168
	s_nop 0
	v_cndmask_b32_e32 v89, v232, v89, vcc
	v_cmp_le_i32_e32 vcc, v82, v151
	v_add_u32_e32 v82, 48, v168
	s_nop 0
	v_cndmask_b32_e32 v106, v232, v106, vcc
	v_cmp_le_i32_e32 vcc, v82, v151
	v_add_u32_e32 v82, 17, v168
	s_nop 0
	v_cndmask_b32_e32 v90, v232, v90, vcc
	v_cmp_le_i32_e32 vcc, v82, v151
	v_add_u32_e32 v82, 49, v168
	s_nop 0
	v_cndmask_b32_e32 v107, v232, v107, vcc
	v_cmp_le_i32_e32 vcc, v82, v151
	v_add_u32_e32 v82, 18, v168
	s_nop 0
	v_cndmask_b32_e32 v91, v232, v91, vcc
	v_cmp_le_i32_e32 vcc, v82, v151
	v_add_u32_e32 v82, 50, v168
	s_nop 0
	v_cndmask_b32_e32 v108, v232, v108, vcc
	v_cmp_le_i32_e32 vcc, v82, v151
	v_add_u32_e32 v82, 19, v168
	s_nop 0
	v_cndmask_b32_e32 v92, v232, v92, vcc
	v_cmp_le_i32_e32 vcc, v82, v151
	v_add_u32_e32 v82, 51, v168
	s_nop 0
	v_cndmask_b32_e32 v109, v232, v109, vcc
	v_cmp_le_i32_e32 vcc, v82, v151
	v_add_u32_e32 v82, 24, v168
	s_nop 0
	v_cndmask_b32_e32 v93, v232, v93, vcc
	v_cmp_le_i32_e32 vcc, v82, v151
	v_add_u32_e32 v82, 56, v168
	s_nop 0
	v_cndmask_b32_e32 v110, v232, v110, vcc
	v_cmp_le_i32_e32 vcc, v82, v151
	v_add_u32_e32 v82, 25, v168
	s_nop 0
	v_cndmask_b32_e32 v94, v232, v94, vcc
	v_cmp_le_i32_e32 vcc, v82, v151
	v_add_u32_e32 v82, 57, v168
	s_nop 0
	v_cndmask_b32_e32 v111, v232, v111, vcc
	v_cmp_le_i32_e32 vcc, v82, v151
	v_add_u32_e32 v82, 26, v168
	s_nop 0
	v_cndmask_b32_e32 v95, v232, v95, vcc
	v_cmp_le_i32_e32 vcc, v82, v151
	v_add_u32_e32 v82, 58, v168
	s_nop 0
	v_cndmask_b32_e32 v173, v232, v112, vcc
	v_cmp_le_i32_e32 vcc, v82, v151
	v_add_u32_e32 v82, 27, v168
	v_exp_f32_e32 v112, v102
	v_cndmask_b32_e32 v174, v232, v96, vcc
	v_cmp_le_i32_e32 vcc, v82, v151
	v_add_u32_e32 v82, 59, v168
	v_exp_f32_e32 v96, v169
	v_cndmask_b32_e32 v175, v232, v113, vcc
	v_cmp_le_i32_e32 vcc, v82, v151
	v_exp_f32_e32 v82, v98
	v_exp_f32_e32 v98, v171
	v_cndmask_b32_e32 v176, v232, v97, vcc
	v_exp_f32_e32 v97, v170
	v_exp_f32_e32 v113, v103
	v_pk_add_f32 v[86:87], v[164:165], v[82:83]
	v_exp_f32_e32 v168, v104
	v_pk_add_f32 v[86:87], v[96:97], v[86:87]
	v_exp_f32_e32 v169, v105
	v_pk_add_f32 v[86:87], v[84:85], v[86:87]
	v_cvt_pk_bf16_f32 v82, v82, v83
	v_pk_add_f32 v[86:87], v[98:99], v[86:87]
	v_cvt_pk_bf16_f32 v83, v84, v85
	v_pk_add_f32 v[86:87], v[112:113], v[86:87]
	v_cvt_pk_bf16_f32 v84, v112, v113
	v_add3_u32 v112, s14, v167, v160
	v_add_u32_e32 v112, v112, v160
	v_pk_add_f32 v[86:87], v[100:101], v[86:87]
	v_add_u32_e32 v113, 0x4000, v112
	v_pk_add_f32 v[86:87], v[168:169], v[86:87]
	v_cvt_pk_bf16_f32 v85, v168, v169
	ds_read_b128 v[168:171], v113 offset:1536
	v_exp_f32_e32 v102, v88
	v_exp_f32_e32 v103, v89
	v_exp_f32_e32 v104, v106
	v_exp_f32_e32 v105, v107
	v_exp_f32_e32 v88, v90
	v_exp_f32_e32 v89, v91
	v_add_u32_e32 v112, 0x3000, v112
	v_exp_f32_e32 v106, v108
	v_exp_f32_e32 v90, v92
	v_exp_f32_e32 v107, v109
	v_exp_f32_e32 v91, v93
	v_exp_f32_e32 v108, v110
	v_exp_f32_e32 v92, v94
	v_exp_f32_e32 v109, v111
	v_exp_f32_e32 v93, v95
	v_exp_f32_e32 v110, v173
	v_exp_f32_e32 v94, v174
	v_exp_f32_e32 v111, v175
	v_exp_f32_e32 v95, v176
	ds_read_b128 v[172:175], v112 offset:1024
	ds_read_b128 v[176:179], v112 offset:1056
	v_pk_add_f32 v[86:87], v[102:103], v[86:87]
	s_waitcnt lgkmcnt(1)
	v_mfma_f32_32x32x16_bf16 v[66:81], v[172:175], v[82:85], v[66:81]
	v_add_f32_e64 v86, v104, v86
	v_add_f32_e64 v87, v105, v87
	s_mov_b64 s[14:15], 0
	v_add_f32_e64 v86, v88, v86
	v_add_f32_e64 v87, v89, v87
	v_pk_add_f32 v[86:87], v[106:107], v[86:87]
	s_nop 0
	v_pk_add_f32 v[86:87], v[90:91], v[86:87]
	v_mfma_f32_32x32x16_bf16 v[50:65], v[168:171], v[82:85], v[50:65]
	v_cvt_pk_bf16_f32 v82, v104, v105
	v_cvt_pk_bf16_f32 v83, v106, v107
	ds_read_b128 v[104:107], v113 offset:1568
	v_cvt_pk_bf16_f32 v84, v108, v109
	v_cvt_pk_bf16_f32 v85, v110, v111
	v_pk_add_f32 v[86:87], v[108:109], v[86:87]
	s_waitcnt lgkmcnt(1)
	v_mfma_f32_32x32x16_bf16 v[66:81], v[176:179], v[82:85], v[66:81]
	v_add_f32_e64 v86, v92, v86
	v_add_f32_e64 v87, v93, v87
	v_add_f32_e64 v86, v110, v86
	v_add_f32_e64 v87, v111, v87
	v_add_f32_e64 v86, v94, v86
	v_add_f32_e64 v87, v95, v87
	s_waitcnt lgkmcnt(0)
	v_mfma_f32_32x32x16_bf16 v[50:65], v[104:107], v[82:85], v[50:65]
	v_cvt_pk_bf16_f32 v82, v96, v97
	v_cvt_pk_bf16_f32 v83, v98, v99
	v_cvt_pk_bf16_f32 v84, v100, v101
	v_cvt_pk_bf16_f32 v85, v102, v103
	ds_read_b128 v[96:99], v112 offset:1088
	ds_read_b128 v[100:103], v113 offset:1600
	s_waitcnt lgkmcnt(1)
	v_mfma_f32_32x32x16_bf16 v[66:81], v[96:99], v[82:85], v[66:81]
	s_waitcnt lgkmcnt(0)
	v_mfma_f32_32x32x16_bf16 v[50:65], v[100:103], v[82:85], v[50:65]
	v_cvt_pk_bf16_f32 v82, v88, v89
	v_cvt_pk_bf16_f32 v83, v90, v91
	v_cvt_pk_bf16_f32 v84, v92, v93
	v_cvt_pk_bf16_f32 v85, v94, v95
	ds_read_b128 v[88:91], v112 offset:1120
	ds_read_b128 v[92:95], v113 offset:1632
	s_waitcnt lgkmcnt(1)
	v_mfma_f32_32x32x16_bf16 v[66:81], v[88:91], v[82:85], v[66:81]
	s_waitcnt lgkmcnt(0)
	v_mfma_f32_32x32x16_bf16 v[50:65], v[92:95], v[82:85], v[50:65]
.LBB0_562:
	s_andn2_b64 vcc, exec, s[14:15]
	s_cbranch_vccnz .LBB0_564
	s_nop 9
	ds_read_b128 v[50:53], v166
	ds_read_b128 v[82:85], v166 offset:6656
	v_lshl_add_u32 v86, s3, 7, v150
	v_cmp_le_i32_e32 vcc, v86, v151
	v_add_u32_e32 v87, 32, v86
	s_waitcnt lgkmcnt(1)
	v_mfma_f32_32x32x16_bf16 v[66:81], v[50:53], v[144:147], v[2:17]
	s_waitcnt lgkmcnt(0)
	v_mfma_f32_32x32x16_bf16 v[50:65], v[82:85], v[144:147], v[2:17]
	ds_read_b128 v[82:85], v166 offset:32
	s_waitcnt lgkmcnt(0)
	v_mfma_f32_32x32x16_bf16 v[66:81], v[82:85], v[140:143], v[66:81]
	ds_read_b128 v[82:85], v166 offset:6688
	s_waitcnt lgkmcnt(0)
	v_mfma_f32_32x32x16_bf16 v[50:65], v[82:85], v[140:143], v[50:65]
	ds_read_b128 v[82:85], v166 offset:64
	s_waitcnt lgkmcnt(0)
	v_mfma_f32_32x32x16_bf16 v[66:81], v[82:85], v[136:139], v[66:81]
	ds_read_b128 v[82:85], v166 offset:6720
	s_waitcnt lgkmcnt(0)
	v_mfma_f32_32x32x16_bf16 v[50:65], v[82:85], v[136:139], v[50:65]
	ds_read_b128 v[82:85], v166 offset:96
	s_waitcnt lgkmcnt(0)
	v_mfma_f32_32x32x16_bf16 v[66:81], v[82:85], v[132:135], v[66:81]
	ds_read_b128 v[82:85], v166 offset:6752
	s_waitcnt lgkmcnt(0)
	v_mfma_f32_32x32x16_bf16 v[50:65], v[82:85], v[132:135], v[50:65]
	ds_read_b128 v[82:85], v166 offset:128
	s_waitcnt lgkmcnt(0)
	v_mfma_f32_32x32x16_bf16 v[66:81], v[82:85], v[128:131], v[66:81]
	ds_read_b128 v[82:85], v166 offset:6784
	s_waitcnt lgkmcnt(0)
	v_mfma_f32_32x32x16_bf16 v[50:65], v[82:85], v[128:131], v[50:65]
	ds_read_b128 v[82:85], v166 offset:160
	s_waitcnt lgkmcnt(0)
	v_mfma_f32_32x32x16_bf16 v[66:81], v[82:85], v[124:127], v[66:81]
	ds_read_b128 v[82:85], v166 offset:6816
	s_waitcnt lgkmcnt(0)
	v_mfma_f32_32x32x16_bf16 v[50:65], v[82:85], v[124:127], v[50:65]
	s_nop 8
	v_cndmask_b32_e32 v66, v232, v66, vcc
	v_cmp_le_i32_e32 vcc, v87, v151
	v_or_b32_e32 v82, 1, v86
	s_nop 0
	v_cndmask_b32_e32 v50, v232, v50, vcc
	v_cmp_le_i32_e32 vcc, v82, v151
	v_add_u32_e32 v82, 33, v86
	s_nop 0
	v_cndmask_b32_e32 v67, v232, v67, vcc
	v_cmp_le_i32_e32 vcc, v82, v151
	v_or_b32_e32 v82, 2, v86
	s_nop 0
	v_cndmask_b32_e32 v51, v232, v51, vcc
	v_cmp_le_i32_e32 vcc, v82, v151
	v_add_u32_e32 v82, 34, v86
	s_nop 0
	v_cndmask_b32_e32 v68, v232, v68, vcc
	v_cmp_le_i32_e32 vcc, v82, v151
	s_nop 1
	v_cndmask_b32_e32 v82, v232, v52, vcc
	v_or_b32_e32 v52, 3, v86
	v_cmp_le_i32_e32 vcc, v52, v151
	v_add_u32_e32 v52, 35, v86
	s_nop 0
	v_cndmask_b32_e32 v69, v232, v69, vcc
	v_cmp_le_i32_e32 vcc, v52, v151
	v_add_u32_e32 v52, 8, v86
	s_nop 0
	v_cndmask_b32_e32 v83, v232, v53, vcc
	v_cmp_le_i32_e32 vcc, v52, v151
	v_add_u32_e32 v52, 40, v86
	v_exp_f32_e32 v53, v51
	v_cndmask_b32_e32 v70, v232, v70, vcc
	v_cmp_le_i32_e32 vcc, v52, v151
	v_add_u32_e32 v52, 9, v86
	v_mul_u32_u24_e32 v51, 0x90, v193
	v_cndmask_b32_e32 v84, v232, v54, vcc
	v_cmp_le_i32_e32 vcc, v52, v151
	v_add_u32_e32 v52, 41, v86
	v_exp_f32_e32 v54, v82
	v_cndmask_b32_e32 v71, v232, v71, vcc
	v_cmp_le_i32_e32 vcc, v52, v151
	v_add_u32_e32 v52, 10, v86
	s_nop 0
	v_cndmask_b32_e32 v85, v232, v55, vcc
	v_cmp_le_i32_e32 vcc, v52, v151
	v_add_u32_e32 v52, 42, v86
	v_exp_f32_e32 v55, v83
	v_cndmask_b32_e32 v72, v232, v72, vcc
	v_cmp_le_i32_e32 vcc, v52, v151
	v_add_u32_e32 v52, 11, v86
	s_nop 0
	v_cndmask_b32_e32 v87, v232, v56, vcc
	v_cmp_le_i32_e32 vcc, v52, v151
	v_add_u32_e32 v52, 43, v86
	v_exp_f32_e32 v56, v68
	v_cndmask_b32_e32 v73, v232, v73, vcc
	v_cmp_le_i32_e32 vcc, v52, v151
	v_add_u32_e32 v52, 16, v86
	s_nop 0
	v_cndmask_b32_e32 v88, v232, v57, vcc
	v_cmp_le_i32_e32 vcc, v52, v151
	v_add_u32_e32 v52, 48, v86
	v_exp_f32_e32 v57, v69
	v_cndmask_b32_e32 v74, v232, v74, vcc
	v_cmp_le_i32_e32 vcc, v52, v151
	v_add_u32_e32 v52, 17, v86
	v_cvt_pk_bf16_f32 v69, v56, v57
	v_cndmask_b32_e32 v89, v232, v58, vcc
	v_cmp_le_i32_e32 vcc, v52, v151
	v_add_u32_e32 v52, 49, v86
	v_exp_f32_e32 v58, v84
	v_cndmask_b32_e32 v90, v232, v75, vcc
	v_cmp_le_i32_e32 vcc, v52, v151
	v_add_u32_e32 v52, 18, v86
	s_nop 0
	v_cndmask_b32_e32 v91, v232, v59, vcc
	v_cmp_le_i32_e32 vcc, v52, v151
	v_add_u32_e32 v52, 50, v86
	v_exp_f32_e32 v59, v85
	v_cndmask_b32_e32 v92, v232, v76, vcc
	v_cmp_le_i32_e32 vcc, v52, v151
	v_add_u32_e32 v52, 19, v86
	v_exp_f32_e32 v76, v66
	v_cndmask_b32_e32 v93, v232, v60, vcc
	v_cmp_le_i32_e32 vcc, v52, v151
	v_add_u32_e32 v52, 51, v86
	v_exp_f32_e32 v60, v70
	v_cndmask_b32_e32 v94, v232, v77, vcc
	v_cmp_le_i32_e32 vcc, v52, v151
	v_add_u32_e32 v52, 24, v86
	v_exp_f32_e32 v77, v67
	v_cndmask_b32_e32 v95, v232, v61, vcc
	v_cmp_le_i32_e32 vcc, v52, v151
	v_add_u32_e32 v52, 56, v86
	v_exp_f32_e32 v61, v71
	v_cndmask_b32_e32 v96, v232, v78, vcc
	v_cmp_le_i32_e32 vcc, v52, v151
	v_add_u32_e32 v52, 25, v86
	v_exp_f32_e32 v78, v74
	v_cndmask_b32_e32 v97, v232, v62, vcc
	v_cmp_le_i32_e32 vcc, v52, v151
	v_add_u32_e32 v52, 57, v86
	v_exp_f32_e32 v62, v72
	v_cndmask_b32_e32 v98, v232, v79, vcc
	v_cmp_le_i32_e32 vcc, v52, v151
	v_add_u32_e32 v52, 26, v86
	v_add3_u32 v72, s16, v51, v160
	v_add_u32_e32 v72, v72, v160
	v_cndmask_b32_e32 v99, v232, v63, vcc
	v_cmp_le_i32_e32 vcc, v52, v151
	v_add_u32_e32 v52, 58, v86
	v_add_u32_e32 v103, 0x3000, v72
	v_cndmask_b32_e32 v100, v232, v80, vcc
	v_cmp_le_i32_e32 vcc, v52, v151
	v_add_u32_e32 v52, 27, v86
	v_add_u32_e32 v104, 0x4000, v72
	v_cndmask_b32_e32 v101, v232, v64, vcc
	v_cmp_le_i32_e32 vcc, v52, v151
	v_add_u32_e32 v52, 59, v86
	v_exp_f32_e32 v63, v73
	v_cndmask_b32_e32 v81, v232, v81, vcc
	v_cmp_le_i32_e32 vcc, v52, v151
	ds_read_b128 v[72:75], v104 offset:1536
	v_cvt_pk_bf16_f32 v68, v76, v77
	v_cndmask_b32_e32 v102, v232, v65, vcc
	ds_read_b128 v[64:67], v103 offset:1024
	v_cvt_pk_bf16_f32 v70, v60, v61
	v_cvt_pk_bf16_f32 v71, v62, v63
	v_exp_f32_e32 v52, v50
	v_exp_f32_e32 v50, v87
	s_waitcnt lgkmcnt(0)
	v_mfma_f32_32x32x16_bf16 v[18:33], v[64:67], v[68:71], v[18:33]
	ds_read_b128 v[64:67], v103 offset:1056
	v_exp_f32_e32 v79, v90
	v_exp_f32_e32 v82, v92
	v_exp_f32_e32 v83, v94
	v_exp_f32_e32 v84, v96
	v_exp_f32_e32 v85, v98
	v_exp_f32_e32 v86, v100
	v_mfma_f32_32x32x16_bf16 v[34:49], v[72:75], v[68:71], v[34:49]
	ds_read_b128 v[72:75], v104 offset:1568
	v_exp_f32_e32 v87, v81
	v_cvt_pk_bf16_f32 v68, v78, v79
	v_cvt_pk_bf16_f32 v69, v82, v83
	v_cvt_pk_bf16_f32 v70, v84, v85
	v_cvt_pk_bf16_f32 v71, v86, v87
	v_pk_add_f32 v[76:77], v[162:163], v[76:77]
	v_exp_f32_e32 v51, v88
	s_waitcnt lgkmcnt(1)
	v_mfma_f32_32x32x16_bf16 v[18:33], v[64:67], v[68:71], v[18:33]
	ds_read_b128 v[64:67], v103 offset:1088
	v_exp_f32_e32 v80, v89
	v_exp_f32_e32 v81, v91
	v_exp_f32_e32 v88, v93
	v_exp_f32_e32 v89, v95
	v_exp_f32_e32 v90, v97
	v_exp_f32_e32 v91, v99
	s_waitcnt lgkmcnt(1)
	v_mfma_f32_32x32x16_bf16 v[34:49], v[72:75], v[68:71], v[34:49]
	ds_read_b128 v[72:75], v104 offset:1600
	v_cvt_pk_bf16_f32 v68, v52, v53
	v_add_f32_e64 v52, v52, v76
	v_add_f32_e64 v53, v53, v77
	v_cvt_pk_bf16_f32 v69, v54, v55
	v_pk_add_f32 v[52:53], v[56:57], v[52:53]
	v_cvt_pk_bf16_f32 v70, v58, v59
	v_pk_add_f32 v[52:53], v[54:55], v[52:53]
	v_cvt_pk_bf16_f32 v71, v50, v51
	v_pk_add_f32 v[52:53], v[60:61], v[52:53]
	v_exp_f32_e32 v92, v101
	v_pk_add_f32 v[52:53], v[58:59], v[52:53]
	s_waitcnt lgkmcnt(1)
	v_mfma_f32_32x32x16_bf16 v[18:33], v[64:67], v[68:71], v[18:33]
	v_add_f32_e64 v56, v62, v52
	v_add_f32_e64 v57, v63, v53
	ds_read_b128 v[52:55], v103 offset:1120
	ds_read_b128 v[60:63], v104 offset:1632
	v_exp_f32_e32 v93, v102
	v_pk_add_f32 v[50:51], v[50:51], v[56:57]
	v_cvt_pk_bf16_f32 v56, v80, v81
	v_cvt_pk_bf16_f32 v57, v88, v89
	s_waitcnt lgkmcnt(2)
	v_mfma_f32_32x32x16_bf16 v[34:49], v[72:75], v[68:71], v[34:49]
	v_cvt_pk_bf16_f32 v58, v90, v91
	v_cvt_pk_bf16_f32 v59, v92, v93
	v_add_f32_e64 v50, v78, v50
	v_add_f32_e64 v51, v79, v51
	v_add_f32_e64 v50, v80, v50
	v_add_f32_e64 v51, v81, v51
	v_pk_add_f32 v[50:51], v[82:83], v[50:51]
	s_waitcnt lgkmcnt(1)
	v_mfma_f32_32x32x16_bf16 v[18:33], v[52:55], v[56:59], v[18:33]
	v_add_f32_e64 v50, v88, v50
	v_add_f32_e64 v51, v89, v51
	v_add_f32_e64 v50, v84, v50
	v_add_f32_e64 v51, v85, v51
	v_add_f32_e64 v50, v90, v50
	v_add_f32_e64 v51, v91, v51
	s_nop 5
	v_mov_b64_e32 v[80:81], v[32:33]
	s_waitcnt lgkmcnt(0)
	v_mfma_f32_32x32x16_bf16 v[34:49], v[60:63], v[56:59], v[34:49]
	v_add_f32_e64 v50, v86, v50
	v_add_f32_e64 v51, v87, v51
	v_mov_b64_e32 v[78:79], v[30:31]
	v_add_f32_e64 v86, v92, v50
	v_add_f32_e64 v87, v93, v51
	v_mov_b64_e32 v[76:77], v[28:29]
	v_mov_b64_e32 v[74:75], v[26:27]
	v_mov_b64_e32 v[72:73], v[24:25]
	v_mov_b64_e32 v[70:71], v[22:23]
	s_nop 2
	v_mov_b64_e32 v[64:65], v[48:49]
	v_mov_b64_e32 v[62:63], v[46:47]
	v_mov_b64_e32 v[60:61], v[44:45]
	v_mov_b64_e32 v[58:59], v[42:43]
	v_mov_b64_e32 v[56:57], v[40:41]
	v_mov_b64_e32 v[54:55], v[38:39]
	v_mov_b64_e32 v[52:53], v[36:37]
	v_mov_b64_e32 v[50:51], v[34:35]
	v_mov_b64_e32 v[68:69], v[20:21]
	v_mov_b64_e32 v[66:67], v[18:19]

.LBB0_569:
	s_or_b64 exec, exec, s[16:17]
	global_load_dwordx4 v[30:33], v[30:31], off offset:128
	s_bitcmp1_b32 s21, 0
	s_cselect_b32 s16, 0xb000, 0
	s_add_i32 s21, s16, 0
	v_add_u32_e32 v34, s21, v188
	s_waitcnt vmcnt(3)
	ds_write_b128 v34, v[18:21]
	v_add_u32_e32 v18, s21, v189
	s_and_saveexec_b64 s[16:17], s[0:1]
	s_xor_b64 s[16:17], exec, s[16:17]
	s_cbranch_execz .LBB0_571
	s_waitcnt vmcnt(2)
	ds_write_b64 v18, v[22:23] offset:13312
	ds_write_b64 v18, v[24:25] offset:13328
	s_waitcnt vmcnt(1)
	ds_write_b128 v34, v[26:29] offset:22528
.LBB0_571:
	s_andn2_saveexec_b64 s[16:17], s[16:17]
	s_cbranch_execz .LBB0_573
	v_lshlrev_b32_e32 v19, 4, v191
	v_add3_u32 v19, v19, v192, s21
	ds_write_b128 v19, v[116:119]
	s_waitcnt vmcnt(2)
	ds_write_b64 v18, v[22:23] offset:13312
	ds_write_b64 v18, v[24:25] offset:13328
	s_waitcnt vmcnt(1)
	ds_write_b128 v34, v[26:29] offset:22528
	ds_write_b128 v19, v[120:123] offset:22528
.LBB0_573:
	s_or_b64 exec, exec, s[16:17]
	s_waitcnt vmcnt(0)
	ds_write_b64 v18, v[30:31] offset:35840
	ds_write_b64 v18, v[32:33] offset:35856

.LBB0_576:
	s_or_b64 exec, exec, s[14:15]
	s_waitcnt vmcnt(0)
	ds_write_b64 v26, v[30:31] offset:35840
	ds_write_b64 v26, v[32:33] offset:35856

.LBB0_583:
	s_or_b64 exec, exec, s[14:15]
	global_load_dwordx4 v[30:33], v[30:31], off offset:128
	s_bitcmp1_b32 s3, 0
	s_cselect_b32 s14, 0xb000, 0
	s_add_i32 s21, s14, 0
	v_add_u32_e32 v36, s21, v188
	s_waitcnt vmcnt(3)
	ds_write_b128 v36, v[26:29]
	v_add_u32_e32 v26, s21, v189
	s_and_saveexec_b64 s[14:15], s[0:1]
	s_xor_b64 s[14:15], exec, s[14:15]
	s_cbranch_execz .LBB0_585
	s_waitcnt vmcnt(2)
	ds_write_b64 v26, v[18:19] offset:13312
	ds_write_b64 v26, v[20:21] offset:13328
	s_waitcnt vmcnt(1)
	ds_write_b128 v36, v[22:25] offset:22528
.LBB0_585:
	s_andn2_saveexec_b64 s[14:15], s[14:15]
	s_cbranch_execz .LBB0_576
	v_add_u32_e32 v27, s21, v190
	ds_write_b128 v27, v[116:119]
	s_waitcnt vmcnt(2)
	ds_write_b64 v26, v[18:19] offset:13312
	ds_write_b64 v26, v[20:21] offset:13328
	s_waitcnt vmcnt(1)
	ds_write_b128 v36, v[22:25] offset:22528
	ds_write_b128 v27, v[120:123] offset:22528
	s_branch .LBB0_576

.LBB0_1297:
	v_lshl_add_u64 v[212:213], s[74:75], 0, v[10:11]
	s_mov_b64 s[20:21], 0x29151000
	v_lshl_add_u64 v[222:223], s[74:75], 0, v[14:15]
	v_lshl_add_u64 v[204:205], v[212:213], 0, s[20:21]
	s_mov_b64 s[20:21], 0xd851000
	v_lshl_add_u64 v[206:207], v[74:75], 0, s[0:1]
	v_lshl_add_u64 v[212:213], v[212:213], 0, s[20:21]
	s_mov_b64 s[20:21], 0x614000
	s_nop 0
	v_lshl_add_u64 v[208:209], v[222:223], 0, s[20:21]
	s_mov_b64 s[20:21], 0x613000
	s_nop 0
	v_lshl_add_u64 v[210:211], v[222:223], 0, s[20:21]
	global_load_dwordx4 v[120:123], v[204:205], off offset:1280
	global_load_dwordx4 v[124:127], v[206:207], off
	global_load_dwordx4 v[128:131], v[206:207], off offset:16
	global_load_dwordx4 v[132:135], v[208:209], off
	global_load_dwordx4 v[136:139], v[208:209], off offset:16
	global_load_dwordx4 v[140:143], v[210:211], off
	global_load_dwordx4 v[144:147], v[210:211], off offset:16
	global_load_dwordx4 v[148:151], v[204:205], off offset:1344
	global_load_dwordx4 v[152:155], v[206:207], off offset:128
	global_load_dwordx4 v[156:159], v[206:207], off offset:144
	global_load_dwordx4 v[160:163], v[208:209], off offset:128
	global_load_dwordx4 v[164:167], v[208:209], off offset:144
	global_load_dwordx4 v[168:171], v[210:211], off offset:128
	global_load_dwordx4 v[172:175], v[210:211], off offset:144
	global_load_dwordx4 v[176:179], v[204:205], off offset:1408
	global_load_dwordx4 v[180:183], v[206:207], off offset:256
	global_load_dwordx4 v[184:187], v[206:207], off offset:272
	global_load_dwordx4 v[188:191], v[208:209], off offset:256
	global_load_dwordx4 v[192:195], v[208:209], off offset:272
	global_load_dwordx4 v[196:199], v[210:211], off offset:256
	global_load_dwordx4 v[200:203], v[210:211], off offset:272
	s_waitcnt vmcnt(14)
	v_lshlrev_b32_e32 v214, 16, v120
	v_and_b32_e32 v215, 0xffff0000, v120
	v_lshlrev_b32_e32 v216, 16, v121
	v_and_b32_e32 v217, 0xffff0000, v121
	v_lshlrev_b32_e32 v218, 16, v122
	v_and_b32_e32 v219, 0xffff0000, v122
	v_lshlrev_b32_e32 v220, 16, v123
	v_and_b32_e32 v221, 0xffff0000, v123
	v_pk_add_f32 v[132:133], v[132:133], 1.0 op_sel_hi:[1,0]
	v_pk_add_f32 v[134:135], v[134:135], 1.0 op_sel_hi:[1,0]
	v_pk_add_f32 v[136:137], v[136:137], 1.0 op_sel_hi:[1,0]
	v_pk_add_f32 v[138:139], v[138:139], 1.0 op_sel_hi:[1,0]
	v_pk_mul_f32 v[132:133], v[124:125], v[132:133]
	v_pk_mul_f32 v[134:135], v[126:127], v[134:135]
	v_pk_mul_f32 v[136:137], v[128:129], v[136:137]
	v_pk_mul_f32 v[138:139], v[130:131], v[138:139]
	v_pk_mul_f32 v[214:215], v[18:19], v[214:215]
	v_pk_mul_f32 v[216:217], v[12:13], v[216:217]
	v_pk_mul_f32 v[218:219], v[18:19], v[218:219]
	v_pk_mul_f32 v[220:221], v[12:13], v[220:221]
	v_pk_fma_f32 v[214:215], v[132:133], v[214:215], v[140:141]
	v_pk_fma_f32 v[216:217], v[134:135], v[216:217], v[142:143]
	v_pk_fma_f32 v[218:219], v[136:137], v[218:219], v[144:145]
	v_pk_fma_f32 v[220:221], v[138:139], v[220:221], v[146:147]
	v_cvt_pk_bf16_f32 v2, v214, v215
	v_cvt_pk_bf16_f32 v3, v216, v217
	v_cvt_pk_bf16_f32 v4, v218, v219
	v_cvt_pk_bf16_f32 v5, v220, v221
	global_store_dwordx4 v[212:213], v[2:5], off
	global_load_dwordx4 v[120:123], v[204:205], off offset:1472
	global_load_dwordx4 v[124:127], v[206:207], off offset:384
	global_load_dwordx4 v[128:131], v[206:207], off offset:400
	global_load_dwordx4 v[132:135], v[208:209], off offset:384
	global_load_dwordx4 v[136:139], v[208:209], off offset:400
	global_load_dwordx4 v[140:143], v[210:211], off offset:384
	global_load_dwordx4 v[144:147], v[210:211], off offset:400
	s_waitcnt vmcnt(15)
	v_lshlrev_b32_e32 v214, 16, v148
	v_and_b32_e32 v215, 0xffff0000, v148
	v_lshlrev_b32_e32 v216, 16, v149
	v_and_b32_e32 v217, 0xffff0000, v149
	v_lshlrev_b32_e32 v218, 16, v150
	v_and_b32_e32 v219, 0xffff0000, v150
	v_lshlrev_b32_e32 v220, 16, v151
	v_and_b32_e32 v221, 0xffff0000, v151
	v_pk_add_f32 v[160:161], v[160:161], 1.0 op_sel_hi:[1,0]
	v_pk_add_f32 v[162:163], v[162:163], 1.0 op_sel_hi:[1,0]
	v_pk_add_f32 v[164:165], v[164:165], 1.0 op_sel_hi:[1,0]
	v_pk_add_f32 v[166:167], v[166:167], 1.0 op_sel_hi:[1,0]
	v_pk_mul_f32 v[160:161], v[152:153], v[160:161]
	v_pk_mul_f32 v[162:163], v[154:155], v[162:163]
	v_pk_mul_f32 v[164:165], v[156:157], v[164:165]
	v_pk_mul_f32 v[166:167], v[158:159], v[166:167]
	v_pk_mul_f32 v[214:215], v[18:19], v[214:215]
	v_pk_mul_f32 v[216:217], v[12:13], v[216:217]
	v_pk_mul_f32 v[218:219], v[18:19], v[218:219]
	v_pk_mul_f32 v[220:221], v[12:13], v[220:221]
	v_pk_fma_f32 v[214:215], v[160:161], v[214:215], v[168:169]
	v_pk_fma_f32 v[216:217], v[162:163], v[216:217], v[170:171]
	v_pk_fma_f32 v[218:219], v[164:165], v[218:219], v[172:173]
	v_pk_fma_f32 v[220:221], v[166:167], v[220:221], v[174:175]
	v_cvt_pk_bf16_f32 v2, v214, v215
	v_cvt_pk_bf16_f32 v3, v216, v217
	v_cvt_pk_bf16_f32 v4, v218, v219
	v_cvt_pk_bf16_f32 v5, v220, v221
	global_store_dwordx4 v[212:213], v[2:5], off offset:64
	global_load_dwordx4 v[148:151], v[204:205], off offset:1536
	global_load_dwordx4 v[152:155], v[206:207], off offset:512
	global_load_dwordx4 v[156:159], v[206:207], off offset:528
	global_load_dwordx4 v[160:163], v[208:209], off offset:512
	global_load_dwordx4 v[164:167], v[208:209], off offset:528
	global_load_dwordx4 v[168:171], v[210:211], off offset:512
	global_load_dwordx4 v[172:175], v[210:211], off offset:528
	s_waitcnt vmcnt(16)
	v_lshlrev_b32_e32 v214, 16, v176
	v_and_b32_e32 v215, 0xffff0000, v176
	v_lshlrev_b32_e32 v216, 16, v177
	v_and_b32_e32 v217, 0xffff0000, v177
	v_lshlrev_b32_e32 v218, 16, v178
	v_and_b32_e32 v219, 0xffff0000, v178
	v_lshlrev_b32_e32 v220, 16, v179
	v_and_b32_e32 v221, 0xffff0000, v179
	v_pk_add_f32 v[188:189], v[188:189], 1.0 op_sel_hi:[1,0]
	v_pk_add_f32 v[190:191], v[190:191], 1.0 op_sel_hi:[1,0]
	v_pk_add_f32 v[192:193], v[192:193], 1.0 op_sel_hi:[1,0]
	v_pk_add_f32 v[194:195], v[194:195], 1.0 op_sel_hi:[1,0]
	v_pk_mul_f32 v[188:189], v[180:181], v[188:189]
	v_pk_mul_f32 v[190:191], v[182:183], v[190:191]
	v_pk_mul_f32 v[192:193], v[184:185], v[192:193]
	v_pk_mul_f32 v[194:195], v[186:187], v[194:195]
	v_pk_mul_f32 v[214:215], v[18:19], v[214:215]
	v_pk_mul_f32 v[216:217], v[12:13], v[216:217]
	v_pk_mul_f32 v[218:219], v[18:19], v[218:219]
	v_pk_mul_f32 v[220:221], v[12:13], v[220:221]
	v_pk_fma_f32 v[214:215], v[188:189], v[214:215], v[196:197]
	v_pk_fma_f32 v[216:217], v[190:191], v[216:217], v[198:199]
	v_pk_fma_f32 v[218:219], v[192:193], v[218:219], v[200:201]
	v_pk_fma_f32 v[220:221], v[194:195], v[220:221], v[202:203]
	v_cvt_pk_bf16_f32 v2, v214, v215
	v_cvt_pk_bf16_f32 v3, v216, v217
	v_cvt_pk_bf16_f32 v4, v218, v219
	v_cvt_pk_bf16_f32 v5, v220, v221
	global_store_dwordx4 v[212:213], v[2:5], off offset:128
	global_load_dwordx4 v[176:179], v[204:205], off offset:1600
	global_load_dwordx4 v[180:183], v[206:207], off offset:640
	global_load_dwordx4 v[184:187], v[206:207], off offset:656
	global_load_dwordx4 v[188:191], v[208:209], off offset:640
	global_load_dwordx4 v[192:195], v[208:209], off offset:656
	global_load_dwordx4 v[196:199], v[210:211], off offset:640
	global_load_dwordx4 v[200:203], v[210:211], off offset:656
	s_waitcnt vmcnt(16)
	v_lshlrev_b32_e32 v214, 16, v120
	v_and_b32_e32 v215, 0xffff0000, v120
	v_lshlrev_b32_e32 v216, 16, v121
	v_and_b32_e32 v217, 0xffff0000, v121
	v_lshlrev_b32_e32 v218, 16, v122
	v_and_b32_e32 v219, 0xffff0000, v122
	v_lshlrev_b32_e32 v220, 16, v123
	v_and_b32_e32 v221, 0xffff0000, v123
	v_pk_add_f32 v[132:133], v[132:133], 1.0 op_sel_hi:[1,0]
	v_pk_add_f32 v[134:135], v[134:135], 1.0 op_sel_hi:[1,0]
	v_pk_add_f32 v[136:137], v[136:137], 1.0 op_sel_hi:[1,0]
	v_pk_add_f32 v[138:139], v[138:139], 1.0 op_sel_hi:[1,0]
	v_pk_mul_f32 v[132:133], v[124:125], v[132:133]
	v_pk_mul_f32 v[134:135], v[126:127], v[134:135]
	v_pk_mul_f32 v[136:137], v[128:129], v[136:137]
	v_pk_mul_f32 v[138:139], v[130:131], v[138:139]
	v_pk_mul_f32 v[214:215], v[18:19], v[214:215]
	v_pk_mul_f32 v[216:217], v[12:13], v[216:217]
	v_pk_mul_f32 v[218:219], v[18:19], v[218:219]
	v_pk_mul_f32 v[220:221], v[12:13], v[220:221]
	v_pk_fma_f32 v[214:215], v[132:133], v[214:215], v[140:141]
	v_pk_fma_f32 v[216:217], v[134:135], v[216:217], v[142:143]
	v_pk_fma_f32 v[218:219], v[136:137], v[218:219], v[144:145]
	v_pk_fma_f32 v[220:221], v[138:139], v[220:221], v[146:147]
	v_cvt_pk_bf16_f32 v2, v214, v215
	v_cvt_pk_bf16_f32 v3, v216, v217
	v_cvt_pk_bf16_f32 v4, v218, v219
	v_cvt_pk_bf16_f32 v5, v220, v221
	global_store_dwordx4 v[212:213], v[2:5], off offset:192
	global_load_dwordx4 v[120:123], v[204:205], off offset:1664
	global_load_dwordx4 v[124:127], v[206:207], off offset:768
	global_load_dwordx4 v[128:131], v[206:207], off offset:784
	global_load_dwordx4 v[132:135], v[208:209], off offset:768
	global_load_dwordx4 v[136:139], v[208:209], off offset:784
	global_load_dwordx4 v[140:143], v[210:211], off offset:768
	global_load_dwordx4 v[144:147], v[210:211], off offset:784
	s_waitcnt vmcnt(16)
	v_lshlrev_b32_e32 v214, 16, v148
	v_and_b32_e32 v215, 0xffff0000, v148
	v_lshlrev_b32_e32 v216, 16, v149
	v_and_b32_e32 v217, 0xffff0000, v149
	v_lshlrev_b32_e32 v218, 16, v150
	v_and_b32_e32 v219, 0xffff0000, v150
	v_lshlrev_b32_e32 v220, 16, v151
	v_and_b32_e32 v221, 0xffff0000, v151
	v_pk_add_f32 v[160:161], v[160:161], 1.0 op_sel_hi:[1,0]
	v_pk_add_f32 v[162:163], v[162:163], 1.0 op_sel_hi:[1,0]
	v_pk_add_f32 v[164:165], v[164:165], 1.0 op_sel_hi:[1,0]
	v_pk_add_f32 v[166:167], v[166:167], 1.0 op_sel_hi:[1,0]
	v_pk_mul_f32 v[160:161], v[152:153], v[160:161]
	v_pk_mul_f32 v[162:163], v[154:155], v[162:163]
	v_pk_mul_f32 v[164:165], v[156:157], v[164:165]
	v_pk_mul_f32 v[166:167], v[158:159], v[166:167]
	v_pk_mul_f32 v[214:215], v[18:19], v[214:215]
	v_pk_mul_f32 v[216:217], v[12:13], v[216:217]
	v_pk_mul_f32 v[218:219], v[18:19], v[218:219]
	v_pk_mul_f32 v[220:221], v[12:13], v[220:221]
	v_pk_fma_f32 v[214:215], v[160:161], v[214:215], v[168:169]
	v_pk_fma_f32 v[216:217], v[162:163], v[216:217], v[170:171]
	v_pk_fma_f32 v[218:219], v[164:165], v[218:219], v[172:173]
	v_pk_fma_f32 v[220:221], v[166:167], v[220:221], v[174:175]
	v_cvt_pk_bf16_f32 v2, v214, v215
	v_cvt_pk_bf16_f32 v3, v216, v217
	v_cvt_pk_bf16_f32 v4, v218, v219
	v_cvt_pk_bf16_f32 v5, v220, v221
	global_store_dwordx4 v[212:213], v[2:5], off offset:256
	global_load_dwordx4 v[148:151], v[204:205], off offset:1728
	global_load_dwordx4 v[152:155], v[206:207], off offset:896
	global_load_dwordx4 v[156:159], v[206:207], off offset:912
	global_load_dwordx4 v[160:163], v[208:209], off offset:896
	global_load_dwordx4 v[164:167], v[208:209], off offset:912
	global_load_dwordx4 v[168:171], v[210:211], off offset:896
	global_load_dwordx4 v[172:175], v[210:211], off offset:912
	s_waitcnt vmcnt(16)
	v_lshlrev_b32_e32 v214, 16, v176
	v_and_b32_e32 v215, 0xffff0000, v176
	v_lshlrev_b32_e32 v216, 16, v177
	v_and_b32_e32 v217, 0xffff0000, v177
	v_lshlrev_b32_e32 v218, 16, v178
	v_and_b32_e32 v219, 0xffff0000, v178
	v_lshlrev_b32_e32 v220, 16, v179
	v_and_b32_e32 v221, 0xffff0000, v179
	v_pk_add_f32 v[188:189], v[188:189], 1.0 op_sel_hi:[1,0]
	v_pk_add_f32 v[190:191], v[190:191], 1.0 op_sel_hi:[1,0]
	v_pk_add_f32 v[192:193], v[192:193], 1.0 op_sel_hi:[1,0]
	v_pk_add_f32 v[194:195], v[194:195], 1.0 op_sel_hi:[1,0]
	v_pk_mul_f32 v[188:189], v[180:181], v[188:189]
	v_pk_mul_f32 v[190:191], v[182:183], v[190:191]
	v_pk_mul_f32 v[192:193], v[184:185], v[192:193]
	v_pk_mul_f32 v[194:195], v[186:187], v[194:195]
	v_pk_mul_f32 v[214:215], v[18:19], v[214:215]
	v_pk_mul_f32 v[216:217], v[12:13], v[216:217]
	v_pk_mul_f32 v[218:219], v[18:19], v[218:219]
	v_pk_mul_f32 v[220:221], v[12:13], v[220:221]
	v_pk_fma_f32 v[214:215], v[188:189], v[214:215], v[196:197]
	v_pk_fma_f32 v[216:217], v[190:191], v[216:217], v[198:199]
	v_pk_fma_f32 v[218:219], v[192:193], v[218:219], v[200:201]
	v_pk_fma_f32 v[220:221], v[194:195], v[220:221], v[202:203]
	v_cvt_pk_bf16_f32 v2, v214, v215
	v_cvt_pk_bf16_f32 v3, v216, v217
	v_cvt_pk_bf16_f32 v4, v218, v219
	v_cvt_pk_bf16_f32 v5, v220, v221
	global_store_dwordx4 v[212:213], v[2:5], off offset:320
	s_waitcnt vmcnt(9)
	v_lshlrev_b32_e32 v214, 16, v120
	v_and_b32_e32 v215, 0xffff0000, v120
	v_lshlrev_b32_e32 v216, 16, v121
	v_and_b32_e32 v217, 0xffff0000, v121
	v_lshlrev_b32_e32 v218, 16, v122
	v_and_b32_e32 v219, 0xffff0000, v122
	v_lshlrev_b32_e32 v220, 16, v123
	v_and_b32_e32 v221, 0xffff0000, v123
	v_pk_add_f32 v[132:133], v[132:133], 1.0 op_sel_hi:[1,0]
	v_pk_add_f32 v[134:135], v[134:135], 1.0 op_sel_hi:[1,0]
	v_pk_add_f32 v[136:137], v[136:137], 1.0 op_sel_hi:[1,0]
	v_pk_add_f32 v[138:139], v[138:139], 1.0 op_sel_hi:[1,0]
	v_pk_mul_f32 v[132:133], v[124:125], v[132:133]
	v_pk_mul_f32 v[134:135], v[126:127], v[134:135]
	v_pk_mul_f32 v[136:137], v[128:129], v[136:137]
	v_pk_mul_f32 v[138:139], v[130:131], v[138:139]
	v_pk_mul_f32 v[214:215], v[18:19], v[214:215]
	v_pk_mul_f32 v[216:217], v[12:13], v[216:217]
	v_pk_mul_f32 v[218:219], v[18:19], v[218:219]
	v_pk_mul_f32 v[220:221], v[12:13], v[220:221]
	v_pk_fma_f32 v[214:215], v[132:133], v[214:215], v[140:141]
	v_pk_fma_f32 v[216:217], v[134:135], v[216:217], v[142:143]
	v_pk_fma_f32 v[218:219], v[136:137], v[218:219], v[144:145]
	v_pk_fma_f32 v[220:221], v[138:139], v[220:221], v[146:147]
	v_cvt_pk_bf16_f32 v2, v214, v215
	v_cvt_pk_bf16_f32 v3, v216, v217
	v_cvt_pk_bf16_f32 v4, v218, v219
	v_cvt_pk_bf16_f32 v5, v220, v221
	global_store_dwordx4 v[212:213], v[2:5], off offset:384
	s_waitcnt vmcnt(2)
	v_lshlrev_b32_e32 v214, 16, v148
	v_and_b32_e32 v215, 0xffff0000, v148
	v_lshlrev_b32_e32 v216, 16, v149
	v_and_b32_e32 v217, 0xffff0000, v149
	v_lshlrev_b32_e32 v218, 16, v150
	v_and_b32_e32 v219, 0xffff0000, v150
	v_lshlrev_b32_e32 v220, 16, v151
	v_and_b32_e32 v221, 0xffff0000, v151
	v_pk_add_f32 v[160:161], v[160:161], 1.0 op_sel_hi:[1,0]
	v_pk_add_f32 v[162:163], v[162:163], 1.0 op_sel_hi:[1,0]
	v_pk_add_f32 v[164:165], v[164:165], 1.0 op_sel_hi:[1,0]
	v_pk_add_f32 v[166:167], v[166:167], 1.0 op_sel_hi:[1,0]
	v_pk_mul_f32 v[160:161], v[152:153], v[160:161]
	v_pk_mul_f32 v[162:163], v[154:155], v[162:163]
	v_pk_mul_f32 v[164:165], v[156:157], v[164:165]
	v_pk_mul_f32 v[166:167], v[158:159], v[166:167]
	v_pk_mul_f32 v[214:215], v[18:19], v[214:215]
	v_pk_mul_f32 v[216:217], v[12:13], v[216:217]
	v_pk_mul_f32 v[218:219], v[18:19], v[218:219]
	v_pk_mul_f32 v[220:221], v[12:13], v[220:221]
	v_pk_fma_f32 v[214:215], v[160:161], v[214:215], v[168:169]
	v_pk_fma_f32 v[216:217], v[162:163], v[216:217], v[170:171]
	v_pk_fma_f32 v[218:219], v[164:165], v[218:219], v[172:173]
	v_pk_fma_f32 v[220:221], v[166:167], v[220:221], v[174:175]
	v_cvt_pk_bf16_f32 v2, v214, v215
	v_cvt_pk_bf16_f32 v3, v216, v217
	v_cvt_pk_bf16_f32 v4, v218, v219
	v_cvt_pk_bf16_f32 v5, v220, v221
	global_store_dwordx4 v[212:213], v[2:5], off offset:448
	s_mov_b64 s[20:21], 0x200
	s_add_u32 s0, s0, 0x400
	v_lshl_add_u64 v[10:11], v[10:11], 0, s[20:21]
	s_mov_b64 s[20:21], 0x400
	s_addc_u32 s1, s1, 0
	v_lshl_add_u64 v[14:15], v[14:15], 0, s[20:21]
	s_cmpk_eq_i32 s0, 0x1000
	s_cbranch_scc0 .LBB0_1297
	s_barrier
	s_and_saveexec_b64 s[0:1], s[42:43]
	s_cbranch_execz .LBB0_1300
	ds_read_b32 v2, v63
	s_waitcnt lgkmcnt(0)
	global_atomic_add v2, v[60:61], v2, off sc0
	s_waitcnt vmcnt(0)
	ds_write_b32 v86, v2

.LBB0_1482:
	s_lshl_b32 s19, s0, 8
	s_and_b32 s19, s19, 0x300
	v_or_b32_e32 v187, s19, v183
	v_add_u32_e32 v152, v181, v1
	s_waitcnt vmcnt(0)
	v_and_b32_e32 v230, 0x80000001, v167
	v_cmp_eq_u32_e32 vcc, 0, v230
	s_and_saveexec_b64 s[38:39], vcc
	v_lshrrev_b32_e32 v230, 1, v167
	v_mov_b32_e32 v231, 0
	v_lshlrev_b64 v[230:231], 10, v[230:231]
	v_or_b32_e32 v230, v230, v187
	v_lshl_add_u64 v[230:231], v[230:231], 1, s[92:93]
	global_load_dwordx4 v[192:195], v[230:231], off
	global_load_dwordx4 v[196:199], v[230:231], off offset:256
	s_or_b64 exec, exec, s[38:39]
	v_and_b32_e32 v230, 0x80000001, v166
	v_cmp_eq_u32_e32 vcc, 0, v230
	s_and_saveexec_b64 s[38:39], vcc
	v_lshrrev_b32_e32 v230, 1, v166
	v_mov_b32_e32 v231, 0
	v_lshlrev_b64 v[230:231], 10, v[230:231]
	v_or_b32_e32 v230, v230, v187
	v_lshl_add_u64 v[230:231], v[230:231], 1, s[92:93]
	global_load_dwordx4 v[200:203], v[230:231], off
	global_load_dwordx4 v[204:207], v[230:231], off offset:256
	s_or_b64 exec, exec, s[38:39]
	v_and_b32_e32 v230, 0x80000001, v173
	v_cmp_eq_u32_e32 vcc, 0, v230
	s_and_saveexec_b64 s[38:39], vcc
	v_lshrrev_b32_e32 v230, 1, v173
	v_mov_b32_e32 v231, 0
	v_lshlrev_b64 v[230:231], 10, v[230:231]
	v_or_b32_e32 v230, v230, v187
	v_lshl_add_u64 v[230:231], v[230:231], 1, s[92:93]
	global_load_dwordx4 v[208:211], v[230:231], off
	global_load_dwordx4 v[212:215], v[230:231], off offset:256
	s_or_b64 exec, exec, s[38:39]
	v_and_b32_e32 v230, 0x80000001, v172
	v_cmp_eq_u32_e32 vcc, 0, v230
	s_and_saveexec_b64 s[38:39], vcc
	v_lshrrev_b32_e32 v230, 1, v172
	v_mov_b32_e32 v231, 0
	v_lshlrev_b64 v[230:231], 10, v[230:231]
	v_or_b32_e32 v230, v230, v187
	v_lshl_add_u64 v[230:231], v[230:231], 1, s[92:93]
	global_load_dwordx4 v[216:219], v[230:231], off
	global_load_dwordx4 v[220:223], v[230:231], off offset:256
	s_or_b64 exec, exec, s[38:39]
	v_and_b32_e32 v230, 0x80000001, v178
	v_cmp_eq_u32_e32 vcc, 0, v230
	s_and_saveexec_b64 s[38:39], vcc
	v_lshrrev_b32_e32 v230, 1, v178
	v_mov_b32_e32 v231, 0
	v_lshlrev_b64 v[230:231], 10, v[230:231]
	v_or_b32_e32 v230, v230, v187
	v_lshl_add_u64 v[230:231], v[230:231], 1, s[92:93]
	global_load_dwordx4 v[234:237], v[230:231], off
	global_load_dwordx4 v[238:241], v[230:231], off offset:256
	s_or_b64 exec, exec, s[38:39]
	v_and_b32_e32 v230, 0x80000001, v177
	v_cmp_eq_u32_e32 vcc, 0, v230
	s_and_saveexec_b64 s[38:39], vcc
	v_lshrrev_b32_e32 v230, 1, v177
	v_mov_b32_e32 v231, 0
	v_lshlrev_b64 v[230:231], 10, v[230:231]
	v_or_b32_e32 v230, v230, v187
	v_lshl_add_u64 v[230:231], v[230:231], 1, s[92:93]
	global_load_dwordx4 v[242:245], v[230:231], off
	global_load_dwordx4 v[246:249], v[230:231], off offset:256
	s_or_b64 exec, exec, s[38:39]
	v_cmp_lt_i32_e32 vcc, -1, v167
	v_ashrrev_i32_e32 v153, 31, v152
	v_lshlrev_b32_e32 v154, 2, v187
	s_and_saveexec_b64 s[34:35], vcc
	s_cbranch_execz .LBB0_1491
	v_lshrrev_b32_e32 v114, 14, v167
	v_mul_u32_u24_e32 v114, 0x1800, v114
	v_lshl_add_u64 v[132:133], v[114:115], 2, s[14:15]
	v_mov_b32_e32 v155, v115
	v_readlane_b32 s36, v253, 38
	v_lshl_add_u64 v[160:161], v[132:133], 0, v[154:155]
	v_readlane_b32 s37, v253, 39
	global_load_dwordx4 v[132:135], v[160:161], off
	global_load_dwordx4 v[136:139], v[160:161], off offset:16
	v_lshl_add_u64 v[156:157], v[152:153], 2, s[36:37]
	global_load_dword v158, v[156:157], off
	v_lshrrev_b32_e32 v156, 1, v167
	v_mov_b32_e32 v157, v115
	v_and_b32_e32 v114, 1, v167
	v_lshlrev_b64 v[156:157], 10, v[156:157]
	v_cmp_eq_u32_e32 vcc, 1, v114
	v_or_b32_e32 v162, v156, v187
	v_mov_b32_e32 v163, v157
	s_waitcnt vmcnt(2)
	v_pk_mul_f32 v[134:135], v[8:9], v[134:135]
	v_pk_mul_f32 v[132:133], v[6:7], v[132:133]
	s_waitcnt vmcnt(1)
	v_pk_mul_f32 v[138:139], v[130:131], v[138:139]
	v_pk_mul_f32 v[168:169], v[128:129], v[136:137]
	s_waitcnt vmcnt(0)
	v_pk_mul_f32 v[164:165], v[158:159], v[134:135] op_sel_hi:[0,1]
	v_pk_mul_f32 v[136:137], v[158:159], v[132:133] op_sel_hi:[0,1]
	v_pk_mul_f32 v[138:139], v[158:159], v[138:139] op_sel_hi:[0,1]
	v_pk_mul_f32 v[132:133], v[158:159], v[168:169] op_sel_hi:[0,1]
	s_and_saveexec_b64 s[38:39], vcc
	s_xor_b64 s[38:39], exec, s[38:39]
	s_cbranch_execz .LBB0_1485
	v_cvt_pk_bf16_f32 v134, v136, v137
	v_cvt_pk_bf16_f32 v135, v164, v165
	v_cvt_pk_bf16_f32 v136, v132, v133
	v_cvt_pk_bf16_f32 v137, v138, v139
	v_lshl_add_u64 v[132:133], v[162:163], 1, s[4:5]
	global_store_dwordx4 v[132:133], v[134:137], off
.LBB0_1485:
	s_andn2_saveexec_b64 s[38:39], s[38:39]
	s_cbranch_execz .LBB0_1487
	v_lshl_add_u64 v[162:163], v[162:163], 1, s[92:93]
	v_lshlrev_b32_e32 v134, 16, v192
	v_and_b32_e32 v135, 0xffff0000, v192
	v_lshlrev_b32_e32 v168, 16, v193
	v_and_b32_e32 v169, 0xffff0000, v193
	v_pk_add_f32 v[164:165], v[164:165], v[168:169]
	v_pk_add_f32 v[134:135], v[136:137], v[134:135]
	v_lshlrev_b32_e32 v136, 16, v194
	v_and_b32_e32 v137, 0xffff0000, v194
	v_lshlrev_b32_e32 v168, 16, v195
	v_and_b32_e32 v169, 0xffff0000, v195
	v_pk_add_f32 v[138:139], v[138:139], v[168:169]
	v_pk_add_f32 v[136:137], v[132:133], v[136:137]
	v_cvt_pk_bf16_f32 v132, v134, v135
	v_cvt_pk_bf16_f32 v133, v164, v165
	v_cvt_pk_bf16_f32 v134, v136, v137
	v_cvt_pk_bf16_f32 v135, v138, v139
	global_store_dwordx4 v[162:163], v[132:135], off

.LBB0_1489:
	s_andn2_saveexec_b64 s[38:39], s[38:39]
	s_cbranch_execz .LBB0_1491
	v_lshl_add_u64 v[162:163], v[156:157], 1, s[92:93]
	v_lshlrev_b32_e32 v134, 16, v196
	v_and_b32_e32 v135, 0xffff0000, v196
	v_lshlrev_b32_e32 v156, 16, v197
	v_and_b32_e32 v157, 0xffff0000, v197
	v_pk_add_f32 v[134:135], v[136:137], v[134:135]
	v_lshlrev_b32_e32 v136, 16, v198
	v_and_b32_e32 v137, 0xffff0000, v198
	v_lshlrev_b32_e32 v158, 16, v199
	v_and_b32_e32 v159, 0xffff0000, v199
	v_pk_add_f32 v[156:157], v[160:161], v[156:157]
	v_pk_add_f32 v[138:139], v[138:139], v[158:159]
	v_pk_add_f32 v[136:137], v[132:133], v[136:137]
	v_cvt_pk_bf16_f32 v132, v134, v135
	v_cvt_pk_bf16_f32 v133, v156, v157
	v_cvt_pk_bf16_f32 v134, v136, v137
	v_cvt_pk_bf16_f32 v135, v138, v139
	global_store_dwordx4 v[162:163], v[132:135], off

.LBB0_1494:
	s_andn2_saveexec_b64 s[38:39], s[38:39]
	s_cbranch_execz .LBB0_1496
	v_lshl_add_u64 v[162:163], v[162:163], 1, s[92:93]
	v_lshlrev_b32_e32 v134, 16, v200
	v_and_b32_e32 v135, 0xffff0000, v200
	v_lshlrev_b32_e32 v168, 16, v201
	v_and_b32_e32 v169, 0xffff0000, v201
	v_pk_add_f32 v[164:165], v[164:165], v[168:169]
	v_pk_add_f32 v[134:135], v[136:137], v[134:135]
	v_lshlrev_b32_e32 v136, 16, v202
	v_and_b32_e32 v137, 0xffff0000, v202
	v_lshlrev_b32_e32 v168, 16, v203
	v_and_b32_e32 v169, 0xffff0000, v203
	v_pk_add_f32 v[138:139], v[138:139], v[168:169]
	v_pk_add_f32 v[136:137], v[132:133], v[136:137]
	v_cvt_pk_bf16_f32 v132, v134, v135
	v_cvt_pk_bf16_f32 v133, v164, v165
	v_cvt_pk_bf16_f32 v134, v136, v137
	v_cvt_pk_bf16_f32 v135, v138, v139
	global_store_dwordx4 v[162:163], v[132:135], off

.LBB0_1498:
	s_andn2_saveexec_b64 s[38:39], s[38:39]
	s_cbranch_execz .LBB0_1500
	v_lshl_add_u64 v[162:163], v[156:157], 1, s[92:93]
	v_lshlrev_b32_e32 v134, 16, v204
	v_and_b32_e32 v135, 0xffff0000, v204
	v_lshlrev_b32_e32 v156, 16, v205
	v_and_b32_e32 v157, 0xffff0000, v205
	v_pk_add_f32 v[134:135], v[136:137], v[134:135]
	v_lshlrev_b32_e32 v136, 16, v206
	v_and_b32_e32 v137, 0xffff0000, v206
	v_lshlrev_b32_e32 v158, 16, v207
	v_and_b32_e32 v159, 0xffff0000, v207
	v_pk_add_f32 v[156:157], v[160:161], v[156:157]
	v_pk_add_f32 v[138:139], v[138:139], v[158:159]
	v_pk_add_f32 v[136:137], v[132:133], v[136:137]
	v_cvt_pk_bf16_f32 v132, v134, v135
	v_cvt_pk_bf16_f32 v133, v156, v157
	v_cvt_pk_bf16_f32 v134, v136, v137
	v_cvt_pk_bf16_f32 v135, v138, v139
	global_store_dwordx4 v[162:163], v[132:135], off
.LBB0_1500:
	s_or_b64 exec, exec, s[34:35]
	v_and_b32_e32 v230, 0x80000001, v180
	v_cmp_eq_u32_e32 vcc, 0, v230
	s_and_saveexec_b64 s[38:39], vcc
	v_lshrrev_b32_e32 v230, 1, v180
	v_mov_b32_e32 v231, 0
	v_lshlrev_b64 v[230:231], 10, v[230:231]
	v_or_b32_e32 v230, v230, v187
	v_lshl_add_u64 v[230:231], v[230:231], 1, s[92:93]
	global_load_dwordx4 v[192:195], v[230:231], off
	global_load_dwordx4 v[196:199], v[230:231], off offset:256
	s_or_b64 exec, exec, s[38:39]
	v_and_b32_e32 v230, 0x80000001, v179
	v_cmp_eq_u32_e32 vcc, 0, v230
	s_and_saveexec_b64 s[38:39], vcc
	v_lshrrev_b32_e32 v230, 1, v179
	v_mov_b32_e32 v231, 0
	v_lshlrev_b64 v[230:231], 10, v[230:231]
	v_or_b32_e32 v230, v230, v187
	v_lshl_add_u64 v[230:231], v[230:231], 1, s[92:93]
	global_load_dwordx4 v[200:203], v[230:231], off
	global_load_dwordx4 v[204:207], v[230:231], off offset:256
	s_or_b64 exec, exec, s[38:39]
	v_cmp_lt_i32_e32 vcc, -1, v173
	s_and_saveexec_b64 s[34:35], vcc
	s_cbranch_execz .LBB0_1509
	v_lshrrev_b32_e32 v114, 14, v173
	v_mul_u32_u24_e32 v114, 0x1800, v114
	v_lshl_add_u64 v[132:133], v[114:115], 2, s[14:15]
	v_mov_b32_e32 v155, v115
	v_readlane_b32 s36, v253, 38
	v_lshl_add_u64 v[160:161], v[132:133], 0, v[154:155]
	v_readlane_b32 s37, v253, 39
	global_load_dwordx4 v[132:135], v[160:161], off
	global_load_dwordx4 v[136:139], v[160:161], off offset:16
	v_lshl_add_u64 v[156:157], v[152:153], 2, s[36:37]
	global_load_dword v158, v[156:157], off offset:128
	v_lshrrev_b32_e32 v156, 1, v173
	v_mov_b32_e32 v157, v115
	v_and_b32_e32 v114, 1, v173
	v_lshlrev_b64 v[156:157], 10, v[156:157]
	v_cmp_eq_u32_e32 vcc, 1, v114
	v_or_b32_e32 v162, v156, v187
	v_mov_b32_e32 v163, v157
	s_waitcnt vmcnt(2)
	v_pk_mul_f32 v[134:135], v[118:119], v[134:135]
	v_pk_mul_f32 v[132:133], v[116:117], v[132:133]
	s_waitcnt vmcnt(1)
	v_pk_mul_f32 v[138:139], v[112:113], v[138:139]
	v_pk_mul_f32 v[168:169], v[110:111], v[136:137]
	s_waitcnt vmcnt(0)
	v_pk_mul_f32 v[164:165], v[158:159], v[134:135] op_sel_hi:[0,1]
	v_pk_mul_f32 v[136:137], v[158:159], v[132:133] op_sel_hi:[0,1]
	v_pk_mul_f32 v[138:139], v[158:159], v[138:139] op_sel_hi:[0,1]
	v_pk_mul_f32 v[132:133], v[158:159], v[168:169] op_sel_hi:[0,1]
	s_and_saveexec_b64 s[38:39], vcc
	s_xor_b64 s[38:39], exec, s[38:39]
	s_cbranch_execz .LBB0_1503
	v_cvt_pk_bf16_f32 v134, v136, v137
	v_cvt_pk_bf16_f32 v135, v164, v165
	v_cvt_pk_bf16_f32 v136, v132, v133
	v_cvt_pk_bf16_f32 v137, v138, v139
	v_lshl_add_u64 v[132:133], v[162:163], 1, s[4:5]
	global_store_dwordx4 v[132:133], v[134:137], off
.LBB0_1503:
	s_andn2_saveexec_b64 s[38:39], s[38:39]
	s_cbranch_execz .LBB0_1505
	v_lshl_add_u64 v[162:163], v[162:163], 1, s[92:93]
	v_lshlrev_b32_e32 v134, 16, v208
	v_and_b32_e32 v135, 0xffff0000, v208
	v_lshlrev_b32_e32 v168, 16, v209
	v_and_b32_e32 v169, 0xffff0000, v209
	v_pk_add_f32 v[164:165], v[164:165], v[168:169]
	v_pk_add_f32 v[134:135], v[136:137], v[134:135]
	v_lshlrev_b32_e32 v136, 16, v210
	v_and_b32_e32 v137, 0xffff0000, v210
	v_lshlrev_b32_e32 v168, 16, v211
	v_and_b32_e32 v169, 0xffff0000, v211
	v_pk_add_f32 v[138:139], v[138:139], v[168:169]
	v_pk_add_f32 v[136:137], v[132:133], v[136:137]
	v_cvt_pk_bf16_f32 v132, v134, v135
	v_cvt_pk_bf16_f32 v133, v164, v165
	v_cvt_pk_bf16_f32 v134, v136, v137
	v_cvt_pk_bf16_f32 v135, v138, v139
	global_store_dwordx4 v[162:163], v[132:135], off

.LBB0_1507:
	s_andn2_saveexec_b64 s[38:39], s[38:39]
	s_cbranch_execz .LBB0_1509
	v_lshl_add_u64 v[162:163], v[156:157], 1, s[92:93]
	v_lshlrev_b32_e32 v134, 16, v212
	v_and_b32_e32 v135, 0xffff0000, v212
	v_lshlrev_b32_e32 v156, 16, v213
	v_and_b32_e32 v157, 0xffff0000, v213
	v_pk_add_f32 v[134:135], v[136:137], v[134:135]
	v_lshlrev_b32_e32 v136, 16, v214
	v_and_b32_e32 v137, 0xffff0000, v214
	v_lshlrev_b32_e32 v158, 16, v215
	v_and_b32_e32 v159, 0xffff0000, v215
	v_pk_add_f32 v[156:157], v[160:161], v[156:157]
	v_pk_add_f32 v[138:139], v[138:139], v[158:159]
	v_pk_add_f32 v[136:137], v[132:133], v[136:137]
	v_cvt_pk_bf16_f32 v132, v134, v135
	v_cvt_pk_bf16_f32 v133, v156, v157
	v_cvt_pk_bf16_f32 v134, v136, v137
	v_cvt_pk_bf16_f32 v135, v138, v139
	global_store_dwordx4 v[162:163], v[132:135], off

.LBB0_1512:
	s_andn2_saveexec_b64 s[38:39], s[38:39]
	s_cbranch_execz .LBB0_1514
	v_lshl_add_u64 v[162:163], v[162:163], 1, s[92:93]
	v_lshlrev_b32_e32 v134, 16, v216
	v_and_b32_e32 v135, 0xffff0000, v216
	v_lshlrev_b32_e32 v168, 16, v217
	v_and_b32_e32 v169, 0xffff0000, v217
	v_pk_add_f32 v[164:165], v[164:165], v[168:169]
	v_pk_add_f32 v[134:135], v[136:137], v[134:135]
	v_lshlrev_b32_e32 v136, 16, v218
	v_and_b32_e32 v137, 0xffff0000, v218
	v_lshlrev_b32_e32 v168, 16, v219
	v_and_b32_e32 v169, 0xffff0000, v219
	v_pk_add_f32 v[138:139], v[138:139], v[168:169]
	v_pk_add_f32 v[136:137], v[132:133], v[136:137]
	v_cvt_pk_bf16_f32 v132, v134, v135
	v_cvt_pk_bf16_f32 v133, v164, v165
	v_cvt_pk_bf16_f32 v134, v136, v137
	v_cvt_pk_bf16_f32 v135, v138, v139
	global_store_dwordx4 v[162:163], v[132:135], off

.LBB0_1516:
	s_andn2_saveexec_b64 s[38:39], s[38:39]
	s_cbranch_execz .LBB0_1518
	v_lshl_add_u64 v[162:163], v[156:157], 1, s[92:93]
	v_lshlrev_b32_e32 v134, 16, v220
	v_and_b32_e32 v135, 0xffff0000, v220
	v_lshlrev_b32_e32 v156, 16, v221
	v_and_b32_e32 v157, 0xffff0000, v221
	v_pk_add_f32 v[134:135], v[136:137], v[134:135]
	v_lshlrev_b32_e32 v136, 16, v222
	v_and_b32_e32 v137, 0xffff0000, v222
	v_lshlrev_b32_e32 v158, 16, v223
	v_and_b32_e32 v159, 0xffff0000, v223
	v_pk_add_f32 v[156:157], v[160:161], v[156:157]
	v_pk_add_f32 v[138:139], v[138:139], v[158:159]
	v_pk_add_f32 v[136:137], v[132:133], v[136:137]
	v_cvt_pk_bf16_f32 v132, v134, v135
	v_cvt_pk_bf16_f32 v133, v156, v157
	v_cvt_pk_bf16_f32 v134, v136, v137
	v_cvt_pk_bf16_f32 v135, v138, v139
	global_store_dwordx4 v[162:163], v[132:135], off

.LBB0_1521:
	s_andn2_saveexec_b64 s[38:39], s[38:39]
	s_cbranch_execz .LBB0_1523
	v_lshl_add_u64 v[162:163], v[162:163], 1, s[92:93]
	v_lshlrev_b32_e32 v134, 16, v234
	v_and_b32_e32 v135, 0xffff0000, v234
	v_lshlrev_b32_e32 v168, 16, v235
	v_and_b32_e32 v169, 0xffff0000, v235
	v_pk_add_f32 v[164:165], v[164:165], v[168:169]
	v_pk_add_f32 v[134:135], v[136:137], v[134:135]
	v_lshlrev_b32_e32 v136, 16, v236
	v_and_b32_e32 v137, 0xffff0000, v236
	v_lshlrev_b32_e32 v168, 16, v237
	v_and_b32_e32 v169, 0xffff0000, v237
	v_pk_add_f32 v[138:139], v[138:139], v[168:169]
	v_pk_add_f32 v[136:137], v[132:133], v[136:137]
	v_cvt_pk_bf16_f32 v132, v134, v135
	v_cvt_pk_bf16_f32 v133, v164, v165
	v_cvt_pk_bf16_f32 v134, v136, v137
	v_cvt_pk_bf16_f32 v135, v138, v139
	global_store_dwordx4 v[162:163], v[132:135], off

.LBB0_1525:
	s_andn2_saveexec_b64 s[38:39], s[38:39]
	s_cbranch_execz .LBB0_1527
	v_lshl_add_u64 v[162:163], v[156:157], 1, s[92:93]
	v_lshlrev_b32_e32 v134, 16, v238
	v_and_b32_e32 v135, 0xffff0000, v238
	v_lshlrev_b32_e32 v156, 16, v239
	v_and_b32_e32 v157, 0xffff0000, v239
	v_pk_add_f32 v[134:135], v[136:137], v[134:135]
	v_lshlrev_b32_e32 v136, 16, v240
	v_and_b32_e32 v137, 0xffff0000, v240
	v_lshlrev_b32_e32 v158, 16, v241
	v_and_b32_e32 v159, 0xffff0000, v241
	v_pk_add_f32 v[156:157], v[160:161], v[156:157]
	v_pk_add_f32 v[138:139], v[138:139], v[158:159]
	v_pk_add_f32 v[136:137], v[132:133], v[136:137]
	v_cvt_pk_bf16_f32 v132, v134, v135
	v_cvt_pk_bf16_f32 v133, v156, v157
	v_cvt_pk_bf16_f32 v134, v136, v137
	v_cvt_pk_bf16_f32 v135, v138, v139
	global_store_dwordx4 v[162:163], v[132:135], off

.LBB0_1530:
	s_andn2_saveexec_b64 s[38:39], s[38:39]
	s_cbranch_execz .LBB0_1532
	v_lshl_add_u64 v[162:163], v[162:163], 1, s[92:93]
	v_lshlrev_b32_e32 v134, 16, v242
	v_and_b32_e32 v135, 0xffff0000, v242
	v_lshlrev_b32_e32 v168, 16, v243
	v_and_b32_e32 v169, 0xffff0000, v243
	v_pk_add_f32 v[164:165], v[164:165], v[168:169]
	v_pk_add_f32 v[134:135], v[136:137], v[134:135]
	v_lshlrev_b32_e32 v136, 16, v244
	v_and_b32_e32 v137, 0xffff0000, v244
	v_lshlrev_b32_e32 v168, 16, v245
	v_and_b32_e32 v169, 0xffff0000, v245
	v_pk_add_f32 v[138:139], v[138:139], v[168:169]
	v_pk_add_f32 v[136:137], v[132:133], v[136:137]
	v_cvt_pk_bf16_f32 v132, v134, v135
	v_cvt_pk_bf16_f32 v133, v164, v165
	v_cvt_pk_bf16_f32 v134, v136, v137
	v_cvt_pk_bf16_f32 v135, v138, v139
	global_store_dwordx4 v[162:163], v[132:135], off

.LBB0_1534:
	s_andn2_saveexec_b64 s[38:39], s[38:39]
	s_cbranch_execz .LBB0_1536
	v_lshl_add_u64 v[162:163], v[156:157], 1, s[92:93]
	v_lshlrev_b32_e32 v134, 16, v246
	v_and_b32_e32 v135, 0xffff0000, v246
	v_lshlrev_b32_e32 v156, 16, v247
	v_and_b32_e32 v157, 0xffff0000, v247
	v_pk_add_f32 v[134:135], v[136:137], v[134:135]
	v_lshlrev_b32_e32 v136, 16, v248
	v_and_b32_e32 v137, 0xffff0000, v248
	v_lshlrev_b32_e32 v158, 16, v249
	v_and_b32_e32 v159, 0xffff0000, v249
	v_pk_add_f32 v[156:157], v[160:161], v[156:157]
	v_pk_add_f32 v[138:139], v[138:139], v[158:159]
	v_pk_add_f32 v[136:137], v[132:133], v[136:137]
	v_cvt_pk_bf16_f32 v132, v134, v135
	v_cvt_pk_bf16_f32 v133, v156, v157
	v_cvt_pk_bf16_f32 v134, v136, v137
	v_cvt_pk_bf16_f32 v135, v138, v139
	global_store_dwordx4 v[162:163], v[132:135], off

.LBB0_1548:
	s_andn2_saveexec_b64 s[38:39], s[38:39]
	s_cbranch_execz .LBB0_1550
	v_lshl_add_u64 v[158:159], v[158:159], 1, s[92:93]
	v_lshlrev_b32_e32 v134, 16, v200
	v_and_b32_e32 v135, 0xffff0000, v200
	v_lshlrev_b32_e32 v162, 16, v201
	v_and_b32_e32 v163, 0xffff0000, v201
	v_pk_add_f32 v[160:161], v[160:161], v[162:163]
	v_pk_add_f32 v[134:135], v[136:137], v[134:135]
	v_lshlrev_b32_e32 v136, 16, v202
	v_and_b32_e32 v137, 0xffff0000, v202
	v_lshlrev_b32_e32 v162, 16, v203
	v_and_b32_e32 v163, 0xffff0000, v203
	v_pk_add_f32 v[138:139], v[138:139], v[162:163]
	v_pk_add_f32 v[136:137], v[132:133], v[136:137]
	v_cvt_pk_bf16_f32 v132, v134, v135
	v_cvt_pk_bf16_f32 v133, v160, v161
	v_cvt_pk_bf16_f32 v134, v136, v137
	v_cvt_pk_bf16_f32 v135, v138, v139
	global_store_dwordx4 v[158:159], v[132:135], off

.LBB0_1552:
	s_andn2_saveexec_b64 s[38:39], s[38:39]
	s_cbranch_execz .LBB0_1554
	v_lshl_add_u64 v[158:159], v[152:153], 1, s[92:93]
	v_lshlrev_b32_e32 v134, 16, v204
	v_and_b32_e32 v135, 0xffff0000, v204
	v_lshlrev_b32_e32 v152, 16, v205
	v_and_b32_e32 v153, 0xffff0000, v205
	v_pk_add_f32 v[134:135], v[136:137], v[134:135]
	v_lshlrev_b32_e32 v136, 16, v206
	v_and_b32_e32 v137, 0xffff0000, v206
	v_lshlrev_b32_e32 v154, 16, v207
	v_and_b32_e32 v155, 0xffff0000, v207
	v_pk_add_f32 v[152:153], v[156:157], v[152:153]
	v_pk_add_f32 v[138:139], v[138:139], v[154:155]
	v_pk_add_f32 v[136:137], v[132:133], v[136:137]
	v_cvt_pk_bf16_f32 v132, v134, v135
	v_cvt_pk_bf16_f32 v133, v152, v153
	v_cvt_pk_bf16_f32 v134, v136, v137
	v_cvt_pk_bf16_f32 v135, v138, v139
	global_store_dwordx4 v[158:159], v[132:135], off
